# padded gather steps no longer exec-masked (fewer per-step instructions) with ring-4 and in-loop scale loads
# speedup vs baseline: 1.0011x; 1.0011x over previous
.Lg1_active:
	s_mov_b32 s46, 0x01010101
	s_mov_b32 s47, 0x01010101
	s_mov_b32 s60, 0x00ff00ff
	s_mov_b32 s61, 0x0c030c01
	v_lshrrev_b32_e32 v107, 3, v1
	v_and_b32_e32 v108, 7, v1
	v_and_b32_e32 v105, 15, v1
	v_lshrrev_b32_e32 v106, 4, v1
	s_bfe_u32 s36, s3, 0x10002
	s_lshl_b32 s58, s36, 3
	s_xor_b32 s59, s58, 8
	v_or_b32_e32 v102, s58, v107
	v_or_b32_e32 v103, s59, v107
	v_lshlrev_b32_e32 v89, 4, v108
	v_and_b32_e32 v90, 56, v1
	v_lshlrev_b32_e32 v90, 2, v90
	s_waitcnt lgkmcnt(0)
	s_lshl_b32 s58, s6, 8
	s_add_u32 s32, s16, s58
	s_addc_u32 s33, s17, 0
	s_lshl_b32 s58, s6, 10
	s_add_u32 s34, s18, s58
	s_addc_u32 s35, s19, 0
	v_lshlrev_b32_e32 v109, 4, v105
	global_load_dword v104, v109, s[32:33] offset:8
	v_lshlrev_b32_e32 v110, 4, v102
	global_load_dwordx2 v[68:69], v110, s[32:33]
	v_lshlrev_b32_e32 v111, 4, v103
	global_load_dwordx2 v[70:71], v111, s[32:33]
	v_lshlrev_b32_e32 v101, 2, v108
	v_lshl_or_b32 v110, v102, 6, v101
	global_load_dword v60, v110, s[34:35]
	global_load_dword v61, v110, s[34:35] offset:32
	v_lshl_or_b32 v111, v103, 6, v101
	global_load_dword v62, v111, s[34:35]
	global_load_dword v63, v111, s[34:35] offset:32
	global_load_dwordx4 v[2:5], v95, s[22:23]
	global_load_dwordx4 v[6:9], v98, s[22:23]
	global_load_dwordx4 v[10:13], v99, s[22:23]
	global_load_dwordx4 v[14:17], v100, s[22:23]
	v_and_b32_e32 v101, 0x7f, v0
	v_lshlrev_b32_e32 v101, 2, v101
	global_load_dword v19, v101, s[24:25]
	s_mul_i32 s48, s3, 0x1100
	s_add_u32 s48, s48, 66048
	v_mul_u32_u24_e32 v91, 0x110, v102
	v_lshl_add_u32 v91, v108, 5, v91
	v_add_u32_e32 v91, s48, v91
	v_mul_u32_u24_e32 v92, 0x110, v103
	v_lshl_add_u32 v92, v108, 5, v92
	v_add_u32_e32 v92, s48, v92
	s_waitcnt vmcnt(5)
	v_readlane_b32 s49, v69, 0
	v_readlane_b32 s50, v69, 8
	v_readlane_b32 s51, v69, 16
	v_readlane_b32 s52, v69, 24
	v_readlane_b32 s53, v69, 32
	v_readlane_b32 s54, v69, 40
	v_readlane_b32 s55, v69, 48
	v_readlane_b32 s56, v69, 56
	s_max_i32 s37, s49, s50
	s_max_i32 s37, s37, s51
	s_max_i32 s37, s37, s52
	s_max_i32 s37, s37, s53
	s_max_i32 s37, s37, s54
	s_max_i32 s37, s37, s55
	s_max_i32 s37, s37, s56
	v_readlane_b32 s49, v71, 0
	v_readlane_b32 s50, v71, 8
	v_readlane_b32 s51, v71, 16
	v_readlane_b32 s52, v71, 24
	v_readlane_b32 s53, v71, 32
	v_readlane_b32 s54, v71, 40
	v_readlane_b32 s55, v71, 48
	v_readlane_b32 s56, v71, 56
	s_max_i32 s38, s49, s50
	s_max_i32 s38, s38, s51
	s_max_i32 s38, s38, s52
	s_max_i32 s38, s38, s53
	s_max_i32 s38, s38, s54
	s_max_i32 s38, s38, s55
	s_max_i32 s38, s38, s56
	v_lshlrev_b32_e32 v103, 9, v104
	v_lshl_or_b32 v103, v106, 5, v103
	s_waitcnt vmcnt(0)
	ds_write_b128 v96, v[2:5]
	ds_write_b128 v96, v[6:9] offset:16384
	ds_write_b128 v96, v[10:13] offset:32768
	ds_write_b128 v96, v[14:17] offset:49152
	v_add_u32_e32 v101, 0x10000, v101
	ds_write_b32 v101, v19
	s_waitcnt lgkmcnt(0)
	s_barrier
	s_mov_b32 s39, 0

.Lg1_sel_done:
	s_min_i32 s40, s41, 32
	s_add_i32 s40, s40, 3
	s_and_b32 s40, s40, 0x3c
	s_max_i32 s40, s40, 4
	v_mov_b32_e32 v2, 0
	v_mov_b32_e32 v3, 0
	v_mov_b32_e32 v4, 0
	v_mov_b32_e32 v5, 0
	v_mov_b32_e32 v6, 0
	v_mov_b32_e32 v7, 0
	v_mov_b32_e32 v8, 0
	v_mov_b32_e32 v9, 0
	v_mov_b32_e32 v10, 0
	v_mov_b32_e32 v11, 0
	v_mov_b32_e32 v12, 0
	v_mov_b32_e32 v13, 0
	v_mov_b32_e32 v14, 0
	v_mov_b32_e32 v15, 0
	v_mov_b32_e32 v16, 0
	v_mov_b32_e32 v17, 0
	v_mov_b32_e32 v18, 0
	s_waitcnt lgkmcnt(0)
	ds_bpermute_b32 v94, v90, v73 offset:0
	ds_bpermute_b32 v95, v90, v73 offset:4
	ds_bpermute_b32 v79, v90, v73 offset:8
	s_waitcnt lgkmcnt(1)
	v_and_b32_e32 v84, 0xffff, v94
	v_lshl_or_b32 v83, v84, 7, v89
	global_load_dwordx4 v[20:23], v83, s[12:13]
	v_lshlrev_b32_e32 v109, 1, v84
	global_load_ushort v52, v109, s[14:15]
	v_lshrrev_b32_e32 v84, 16, v94
	v_lshl_or_b32 v83, v84, 7, v89
	global_load_dwordx4 v[24:27], v83, s[12:13]
	v_lshlrev_b32_e32 v109, 1, v84
	global_load_ushort v53, v109, s[14:15]
	v_and_b32_e32 v84, 0xffff, v95
	v_lshl_or_b32 v83, v84, 7, v89
	global_load_dwordx4 v[28:31], v83, s[12:13]
	v_lshlrev_b32_e32 v109, 1, v84
	global_load_ushort v54, v109, s[14:15]
	v_lshrrev_b32_e32 v84, 16, v95
	v_lshl_or_b32 v83, v84, 7, v89
	global_load_dwordx4 v[32:35], v83, s[12:13]
	v_lshlrev_b32_e32 v109, 1, v84
	global_load_ushort v55, v109, s[14:15]
	s_cmp_le_u32 s40, 4
	s_cbranch_scc1 .Lg1_tail0
	s_waitcnt lgkmcnt(0)
	ds_bpermute_b32 v80, v90, v73 offset:12
	s_waitcnt vmcnt(6)
	v_cvt_f32_f16_e32 v52, v52
	v_cvt_f32_ubyte0_e32 v85, v20
	v_cvt_f32_ubyte1_e32 v86, v20
	v_cvt_f32_ubyte2_e32 v87, v20
	v_cvt_f32_ubyte3_e32 v88, v20
	v_fmac_f32_e32 v2, v85, v52
	v_fmac_f32_e32 v3, v86, v52
	v_fmac_f32_e32 v4, v87, v52
	v_fmac_f32_e32 v5, v88, v52
	v_cvt_f32_ubyte0_e32 v85, v21
	v_cvt_f32_ubyte1_e32 v86, v21
	v_cvt_f32_ubyte2_e32 v87, v21
	v_cvt_f32_ubyte3_e32 v88, v21
	v_fmac_f32_e32 v6, v85, v52
	v_fmac_f32_e32 v7, v86, v52
	v_fmac_f32_e32 v8, v87, v52
	v_fmac_f32_e32 v9, v88, v52
	v_cvt_f32_ubyte0_e32 v85, v22
	v_cvt_f32_ubyte1_e32 v86, v22
	v_cvt_f32_ubyte2_e32 v87, v22
	v_cvt_f32_ubyte3_e32 v88, v22
	v_fmac_f32_e32 v10, v85, v52
	v_fmac_f32_e32 v11, v86, v52
	v_fmac_f32_e32 v12, v87, v52
	v_fmac_f32_e32 v13, v88, v52
	v_cvt_f32_ubyte0_e32 v85, v23
	v_cvt_f32_ubyte1_e32 v86, v23
	v_cvt_f32_ubyte2_e32 v87, v23
	v_cvt_f32_ubyte3_e32 v88, v23
	v_fmac_f32_e32 v14, v85, v52
	v_fmac_f32_e32 v15, v86, v52
	v_fmac_f32_e32 v16, v87, v52
	v_fmac_f32_e32 v17, v88, v52
	v_add_f32_e32 v18, v18, v52
	v_and_b32_e32 v84, 0xffff, v79
	v_lshl_or_b32 v83, v84, 7, v89
	global_load_dwordx4 v[20:23], v83, s[12:13]
	v_lshlrev_b32_e32 v109, 1, v84
	global_load_ushort v52, v109, s[14:15]
	s_waitcnt vmcnt(6)
	v_cvt_f32_f16_e32 v53, v53
	v_cvt_f32_ubyte0_e32 v85, v24
	v_cvt_f32_ubyte1_e32 v86, v24
	v_cvt_f32_ubyte2_e32 v87, v24
	v_cvt_f32_ubyte3_e32 v88, v24
	v_fmac_f32_e32 v2, v85, v53
	v_fmac_f32_e32 v3, v86, v53
	v_fmac_f32_e32 v4, v87, v53
	v_fmac_f32_e32 v5, v88, v53
	v_cvt_f32_ubyte0_e32 v85, v25
	v_cvt_f32_ubyte1_e32 v86, v25
	v_cvt_f32_ubyte2_e32 v87, v25
	v_cvt_f32_ubyte3_e32 v88, v25
	v_fmac_f32_e32 v6, v85, v53
	v_fmac_f32_e32 v7, v86, v53
	v_fmac_f32_e32 v8, v87, v53
	v_fmac_f32_e32 v9, v88, v53
	v_cvt_f32_ubyte0_e32 v85, v26
	v_cvt_f32_ubyte1_e32 v86, v26
	v_cvt_f32_ubyte2_e32 v87, v26
	v_cvt_f32_ubyte3_e32 v88, v26
	v_fmac_f32_e32 v10, v85, v53
	v_fmac_f32_e32 v11, v86, v53
	v_fmac_f32_e32 v12, v87, v53
	v_fmac_f32_e32 v13, v88, v53
	v_cvt_f32_ubyte0_e32 v85, v27
	v_cvt_f32_ubyte1_e32 v86, v27
	v_cvt_f32_ubyte2_e32 v87, v27
	v_cvt_f32_ubyte3_e32 v88, v27
	v_fmac_f32_e32 v14, v85, v53
	v_fmac_f32_e32 v15, v86, v53
	v_fmac_f32_e32 v16, v87, v53
	v_fmac_f32_e32 v17, v88, v53
	v_add_f32_e32 v18, v18, v53
	v_lshrrev_b32_e32 v84, 16, v79
	v_lshl_or_b32 v83, v84, 7, v89
	global_load_dwordx4 v[24:27], v83, s[12:13]
	v_lshlrev_b32_e32 v109, 1, v84
	global_load_ushort v53, v109, s[14:15]
	s_waitcnt lgkmcnt(0)
	ds_bpermute_b32 v79, v90, v73 offset:16
	s_waitcnt vmcnt(6)
	v_cvt_f32_f16_e32 v54, v54
	v_cvt_f32_ubyte0_e32 v85, v28
	v_cvt_f32_ubyte1_e32 v86, v28
	v_cvt_f32_ubyte2_e32 v87, v28
	v_cvt_f32_ubyte3_e32 v88, v28
	v_fmac_f32_e32 v2, v85, v54
	v_fmac_f32_e32 v3, v86, v54
	v_fmac_f32_e32 v4, v87, v54
	v_fmac_f32_e32 v5, v88, v54
	v_cvt_f32_ubyte0_e32 v85, v29
	v_cvt_f32_ubyte1_e32 v86, v29
	v_cvt_f32_ubyte2_e32 v87, v29
	v_cvt_f32_ubyte3_e32 v88, v29
	v_fmac_f32_e32 v6, v85, v54
	v_fmac_f32_e32 v7, v86, v54
	v_fmac_f32_e32 v8, v87, v54
	v_fmac_f32_e32 v9, v88, v54
	v_cvt_f32_ubyte0_e32 v85, v30
	v_cvt_f32_ubyte1_e32 v86, v30
	v_cvt_f32_ubyte2_e32 v87, v30
	v_cvt_f32_ubyte3_e32 v88, v30
	v_fmac_f32_e32 v10, v85, v54
	v_fmac_f32_e32 v11, v86, v54
	v_fmac_f32_e32 v12, v87, v54
	v_fmac_f32_e32 v13, v88, v54
	v_cvt_f32_ubyte0_e32 v85, v31
	v_cvt_f32_ubyte1_e32 v86, v31
	v_cvt_f32_ubyte2_e32 v87, v31
	v_cvt_f32_ubyte3_e32 v88, v31
	v_fmac_f32_e32 v14, v85, v54
	v_fmac_f32_e32 v15, v86, v54
	v_fmac_f32_e32 v16, v87, v54
	v_fmac_f32_e32 v17, v88, v54
	v_add_f32_e32 v18, v18, v54
	v_and_b32_e32 v84, 0xffff, v80
	v_lshl_or_b32 v83, v84, 7, v89
	global_load_dwordx4 v[28:31], v83, s[12:13]
	v_lshlrev_b32_e32 v109, 1, v84
	global_load_ushort v54, v109, s[14:15]
	s_waitcnt vmcnt(6)
	v_cvt_f32_f16_e32 v55, v55
	v_cvt_f32_ubyte0_e32 v85, v32
	v_cvt_f32_ubyte1_e32 v86, v32
	v_cvt_f32_ubyte2_e32 v87, v32
	v_cvt_f32_ubyte3_e32 v88, v32
	v_fmac_f32_e32 v2, v85, v55
	v_fmac_f32_e32 v3, v86, v55
	v_fmac_f32_e32 v4, v87, v55
	v_fmac_f32_e32 v5, v88, v55
	v_cvt_f32_ubyte0_e32 v85, v33
	v_cvt_f32_ubyte1_e32 v86, v33
	v_cvt_f32_ubyte2_e32 v87, v33
	v_cvt_f32_ubyte3_e32 v88, v33
	v_fmac_f32_e32 v6, v85, v55
	v_fmac_f32_e32 v7, v86, v55
	v_fmac_f32_e32 v8, v87, v55
	v_fmac_f32_e32 v9, v88, v55
	v_cvt_f32_ubyte0_e32 v85, v34
	v_cvt_f32_ubyte1_e32 v86, v34
	v_cvt_f32_ubyte2_e32 v87, v34
	v_cvt_f32_ubyte3_e32 v88, v34
	v_fmac_f32_e32 v10, v85, v55
	v_fmac_f32_e32 v11, v86, v55
	v_fmac_f32_e32 v12, v87, v55
	v_fmac_f32_e32 v13, v88, v55
	v_cvt_f32_ubyte0_e32 v85, v35
	v_cvt_f32_ubyte1_e32 v86, v35
	v_cvt_f32_ubyte2_e32 v87, v35
	v_cvt_f32_ubyte3_e32 v88, v35
	v_fmac_f32_e32 v14, v85, v55
	v_fmac_f32_e32 v15, v86, v55
	v_fmac_f32_e32 v16, v87, v55
	v_fmac_f32_e32 v17, v88, v55
	v_add_f32_e32 v18, v18, v55
	v_lshrrev_b32_e32 v84, 16, v80
	v_lshl_or_b32 v83, v84, 7, v89
	global_load_dwordx4 v[32:35], v83, s[12:13]
	v_lshlrev_b32_e32 v109, 1, v84
	global_load_ushort v55, v109, s[14:15]
	s_cmp_le_u32 s40, 8
	s_cbranch_scc1 .Lg1_tail0
	s_waitcnt lgkmcnt(0)
	ds_bpermute_b32 v80, v90, v73 offset:20
	s_waitcnt vmcnt(6)
	v_cvt_f32_f16_e32 v52, v52
	v_cvt_f32_ubyte0_e32 v85, v20
	v_cvt_f32_ubyte1_e32 v86, v20
	v_cvt_f32_ubyte2_e32 v87, v20
	v_cvt_f32_ubyte3_e32 v88, v20
	v_fmac_f32_e32 v2, v85, v52
	v_fmac_f32_e32 v3, v86, v52
	v_fmac_f32_e32 v4, v87, v52
	v_fmac_f32_e32 v5, v88, v52
	v_cvt_f32_ubyte0_e32 v85, v21
	v_cvt_f32_ubyte1_e32 v86, v21
	v_cvt_f32_ubyte2_e32 v87, v21
	v_cvt_f32_ubyte3_e32 v88, v21
	v_fmac_f32_e32 v6, v85, v52
	v_fmac_f32_e32 v7, v86, v52
	v_fmac_f32_e32 v8, v87, v52
	v_fmac_f32_e32 v9, v88, v52
	v_cvt_f32_ubyte0_e32 v85, v22
	v_cvt_f32_ubyte1_e32 v86, v22
	v_cvt_f32_ubyte2_e32 v87, v22
	v_cvt_f32_ubyte3_e32 v88, v22
	v_fmac_f32_e32 v10, v85, v52
	v_fmac_f32_e32 v11, v86, v52
	v_fmac_f32_e32 v12, v87, v52
	v_fmac_f32_e32 v13, v88, v52
	v_cvt_f32_ubyte0_e32 v85, v23
	v_cvt_f32_ubyte1_e32 v86, v23
	v_cvt_f32_ubyte2_e32 v87, v23
	v_cvt_f32_ubyte3_e32 v88, v23
	v_fmac_f32_e32 v14, v85, v52
	v_fmac_f32_e32 v15, v86, v52
	v_fmac_f32_e32 v16, v87, v52
	v_fmac_f32_e32 v17, v88, v52
	v_add_f32_e32 v18, v18, v52
	v_and_b32_e32 v84, 0xffff, v79
	v_lshl_or_b32 v83, v84, 7, v89
	global_load_dwordx4 v[20:23], v83, s[12:13]
	v_lshlrev_b32_e32 v109, 1, v84
	global_load_ushort v52, v109, s[14:15]
	s_waitcnt vmcnt(6)
	v_cvt_f32_f16_e32 v53, v53
	v_cvt_f32_ubyte0_e32 v85, v24
	v_cvt_f32_ubyte1_e32 v86, v24
	v_cvt_f32_ubyte2_e32 v87, v24
	v_cvt_f32_ubyte3_e32 v88, v24
	v_fmac_f32_e32 v2, v85, v53
	v_fmac_f32_e32 v3, v86, v53
	v_fmac_f32_e32 v4, v87, v53
	v_fmac_f32_e32 v5, v88, v53
	v_cvt_f32_ubyte0_e32 v85, v25
	v_cvt_f32_ubyte1_e32 v86, v25
	v_cvt_f32_ubyte2_e32 v87, v25
	v_cvt_f32_ubyte3_e32 v88, v25
	v_fmac_f32_e32 v6, v85, v53
	v_fmac_f32_e32 v7, v86, v53
	v_fmac_f32_e32 v8, v87, v53
	v_fmac_f32_e32 v9, v88, v53
	v_cvt_f32_ubyte0_e32 v85, v26
	v_cvt_f32_ubyte1_e32 v86, v26
	v_cvt_f32_ubyte2_e32 v87, v26
	v_cvt_f32_ubyte3_e32 v88, v26
	v_fmac_f32_e32 v10, v85, v53
	v_fmac_f32_e32 v11, v86, v53
	v_fmac_f32_e32 v12, v87, v53
	v_fmac_f32_e32 v13, v88, v53
	v_cvt_f32_ubyte0_e32 v85, v27
	v_cvt_f32_ubyte1_e32 v86, v27
	v_cvt_f32_ubyte2_e32 v87, v27
	v_cvt_f32_ubyte3_e32 v88, v27
	v_fmac_f32_e32 v14, v85, v53
	v_fmac_f32_e32 v15, v86, v53
	v_fmac_f32_e32 v16, v87, v53
	v_fmac_f32_e32 v17, v88, v53
	v_add_f32_e32 v18, v18, v53
	v_lshrrev_b32_e32 v84, 16, v79
	v_lshl_or_b32 v83, v84, 7, v89
	global_load_dwordx4 v[24:27], v83, s[12:13]
	v_lshlrev_b32_e32 v109, 1, v84
	global_load_ushort v53, v109, s[14:15]
	s_waitcnt lgkmcnt(0)
	ds_bpermute_b32 v79, v90, v73 offset:24
	s_waitcnt vmcnt(6)
	v_cvt_f32_f16_e32 v54, v54
	v_cvt_f32_ubyte0_e32 v85, v28
	v_cvt_f32_ubyte1_e32 v86, v28
	v_cvt_f32_ubyte2_e32 v87, v28
	v_cvt_f32_ubyte3_e32 v88, v28
	v_fmac_f32_e32 v2, v85, v54
	v_fmac_f32_e32 v3, v86, v54
	v_fmac_f32_e32 v4, v87, v54
	v_fmac_f32_e32 v5, v88, v54
	v_cvt_f32_ubyte0_e32 v85, v29
	v_cvt_f32_ubyte1_e32 v86, v29
	v_cvt_f32_ubyte2_e32 v87, v29
	v_cvt_f32_ubyte3_e32 v88, v29
	v_fmac_f32_e32 v6, v85, v54
	v_fmac_f32_e32 v7, v86, v54
	v_fmac_f32_e32 v8, v87, v54
	v_fmac_f32_e32 v9, v88, v54
	v_cvt_f32_ubyte0_e32 v85, v30
	v_cvt_f32_ubyte1_e32 v86, v30
	v_cvt_f32_ubyte2_e32 v87, v30
	v_cvt_f32_ubyte3_e32 v88, v30
	v_fmac_f32_e32 v10, v85, v54
	v_fmac_f32_e32 v11, v86, v54
	v_fmac_f32_e32 v12, v87, v54
	v_fmac_f32_e32 v13, v88, v54
	v_cvt_f32_ubyte0_e32 v85, v31
	v_cvt_f32_ubyte1_e32 v86, v31
	v_cvt_f32_ubyte2_e32 v87, v31
	v_cvt_f32_ubyte3_e32 v88, v31
	v_fmac_f32_e32 v14, v85, v54
	v_fmac_f32_e32 v15, v86, v54
	v_fmac_f32_e32 v16, v87, v54
	v_fmac_f32_e32 v17, v88, v54
	v_add_f32_e32 v18, v18, v54
	v_and_b32_e32 v84, 0xffff, v80
	v_lshl_or_b32 v83, v84, 7, v89
	global_load_dwordx4 v[28:31], v83, s[12:13]
	v_lshlrev_b32_e32 v109, 1, v84
	global_load_ushort v54, v109, s[14:15]
	s_waitcnt vmcnt(6)
	v_cvt_f32_f16_e32 v55, v55
	v_cvt_f32_ubyte0_e32 v85, v32
	v_cvt_f32_ubyte1_e32 v86, v32
	v_cvt_f32_ubyte2_e32 v87, v32
	v_cvt_f32_ubyte3_e32 v88, v32
	v_fmac_f32_e32 v2, v85, v55
	v_fmac_f32_e32 v3, v86, v55
	v_fmac_f32_e32 v4, v87, v55
	v_fmac_f32_e32 v5, v88, v55
	v_cvt_f32_ubyte0_e32 v85, v33
	v_cvt_f32_ubyte1_e32 v86, v33
	v_cvt_f32_ubyte2_e32 v87, v33
	v_cvt_f32_ubyte3_e32 v88, v33
	v_fmac_f32_e32 v6, v85, v55
	v_fmac_f32_e32 v7, v86, v55
	v_fmac_f32_e32 v8, v87, v55
	v_fmac_f32_e32 v9, v88, v55
	v_cvt_f32_ubyte0_e32 v85, v34
	v_cvt_f32_ubyte1_e32 v86, v34
	v_cvt_f32_ubyte2_e32 v87, v34
	v_cvt_f32_ubyte3_e32 v88, v34
	v_fmac_f32_e32 v10, v85, v55
	v_fmac_f32_e32 v11, v86, v55
	v_fmac_f32_e32 v12, v87, v55
	v_fmac_f32_e32 v13, v88, v55
	v_cvt_f32_ubyte0_e32 v85, v35
	v_cvt_f32_ubyte1_e32 v86, v35
	v_cvt_f32_ubyte2_e32 v87, v35
	v_cvt_f32_ubyte3_e32 v88, v35
	v_fmac_f32_e32 v14, v85, v55
	v_fmac_f32_e32 v15, v86, v55
	v_fmac_f32_e32 v16, v87, v55
	v_fmac_f32_e32 v17, v88, v55
	v_add_f32_e32 v18, v18, v55
	v_lshrrev_b32_e32 v84, 16, v80
	v_lshl_or_b32 v83, v84, 7, v89
	global_load_dwordx4 v[32:35], v83, s[12:13]
	v_lshlrev_b32_e32 v109, 1, v84
	global_load_ushort v55, v109, s[14:15]
	s_cmp_le_u32 s40, 12
	s_cbranch_scc1 .Lg1_tail0
	s_waitcnt lgkmcnt(0)
	ds_bpermute_b32 v80, v90, v73 offset:28
	s_waitcnt vmcnt(6)
	v_cvt_f32_f16_e32 v52, v52
	v_cvt_f32_ubyte0_e32 v85, v20
	v_cvt_f32_ubyte1_e32 v86, v20
	v_cvt_f32_ubyte2_e32 v87, v20
	v_cvt_f32_ubyte3_e32 v88, v20
	v_fmac_f32_e32 v2, v85, v52
	v_fmac_f32_e32 v3, v86, v52
	v_fmac_f32_e32 v4, v87, v52
	v_fmac_f32_e32 v5, v88, v52
	v_cvt_f32_ubyte0_e32 v85, v21
	v_cvt_f32_ubyte1_e32 v86, v21
	v_cvt_f32_ubyte2_e32 v87, v21
	v_cvt_f32_ubyte3_e32 v88, v21
	v_fmac_f32_e32 v6, v85, v52
	v_fmac_f32_e32 v7, v86, v52
	v_fmac_f32_e32 v8, v87, v52
	v_fmac_f32_e32 v9, v88, v52
	v_cvt_f32_ubyte0_e32 v85, v22
	v_cvt_f32_ubyte1_e32 v86, v22
	v_cvt_f32_ubyte2_e32 v87, v22
	v_cvt_f32_ubyte3_e32 v88, v22
	v_fmac_f32_e32 v10, v85, v52
	v_fmac_f32_e32 v11, v86, v52
	v_fmac_f32_e32 v12, v87, v52
	v_fmac_f32_e32 v13, v88, v52
	v_cvt_f32_ubyte0_e32 v85, v23
	v_cvt_f32_ubyte1_e32 v86, v23
	v_cvt_f32_ubyte2_e32 v87, v23
	v_cvt_f32_ubyte3_e32 v88, v23
	v_fmac_f32_e32 v14, v85, v52
	v_fmac_f32_e32 v15, v86, v52
	v_fmac_f32_e32 v16, v87, v52
	v_fmac_f32_e32 v17, v88, v52
	v_add_f32_e32 v18, v18, v52
	v_and_b32_e32 v84, 0xffff, v79
	v_lshl_or_b32 v83, v84, 7, v89
	global_load_dwordx4 v[20:23], v83, s[12:13]
	v_lshlrev_b32_e32 v109, 1, v84
	global_load_ushort v52, v109, s[14:15]
	s_waitcnt vmcnt(6)
	v_cvt_f32_f16_e32 v53, v53
	v_cvt_f32_ubyte0_e32 v85, v24
	v_cvt_f32_ubyte1_e32 v86, v24
	v_cvt_f32_ubyte2_e32 v87, v24
	v_cvt_f32_ubyte3_e32 v88, v24
	v_fmac_f32_e32 v2, v85, v53
	v_fmac_f32_e32 v3, v86, v53
	v_fmac_f32_e32 v4, v87, v53
	v_fmac_f32_e32 v5, v88, v53
	v_cvt_f32_ubyte0_e32 v85, v25
	v_cvt_f32_ubyte1_e32 v86, v25
	v_cvt_f32_ubyte2_e32 v87, v25
	v_cvt_f32_ubyte3_e32 v88, v25
	v_fmac_f32_e32 v6, v85, v53
	v_fmac_f32_e32 v7, v86, v53
	v_fmac_f32_e32 v8, v87, v53
	v_fmac_f32_e32 v9, v88, v53
	v_cvt_f32_ubyte0_e32 v85, v26
	v_cvt_f32_ubyte1_e32 v86, v26
	v_cvt_f32_ubyte2_e32 v87, v26
	v_cvt_f32_ubyte3_e32 v88, v26
	v_fmac_f32_e32 v10, v85, v53
	v_fmac_f32_e32 v11, v86, v53
	v_fmac_f32_e32 v12, v87, v53
	v_fmac_f32_e32 v13, v88, v53
	v_cvt_f32_ubyte0_e32 v85, v27
	v_cvt_f32_ubyte1_e32 v86, v27
	v_cvt_f32_ubyte2_e32 v87, v27
	v_cvt_f32_ubyte3_e32 v88, v27
	v_fmac_f32_e32 v14, v85, v53
	v_fmac_f32_e32 v15, v86, v53
	v_fmac_f32_e32 v16, v87, v53
	v_fmac_f32_e32 v17, v88, v53
	v_add_f32_e32 v18, v18, v53
	v_lshrrev_b32_e32 v84, 16, v79
	v_lshl_or_b32 v83, v84, 7, v89
	global_load_dwordx4 v[24:27], v83, s[12:13]
	v_lshlrev_b32_e32 v109, 1, v84
	global_load_ushort v53, v109, s[14:15]
	s_waitcnt lgkmcnt(0)
	ds_bpermute_b32 v79, v90, v74 offset:0
	s_waitcnt vmcnt(6)
	v_cvt_f32_f16_e32 v54, v54
	v_cvt_f32_ubyte0_e32 v85, v28
	v_cvt_f32_ubyte1_e32 v86, v28
	v_cvt_f32_ubyte2_e32 v87, v28
	v_cvt_f32_ubyte3_e32 v88, v28
	v_fmac_f32_e32 v2, v85, v54
	v_fmac_f32_e32 v3, v86, v54
	v_fmac_f32_e32 v4, v87, v54
	v_fmac_f32_e32 v5, v88, v54
	v_cvt_f32_ubyte0_e32 v85, v29
	v_cvt_f32_ubyte1_e32 v86, v29
	v_cvt_f32_ubyte2_e32 v87, v29
	v_cvt_f32_ubyte3_e32 v88, v29
	v_fmac_f32_e32 v6, v85, v54
	v_fmac_f32_e32 v7, v86, v54
	v_fmac_f32_e32 v8, v87, v54
	v_fmac_f32_e32 v9, v88, v54
	v_cvt_f32_ubyte0_e32 v85, v30
	v_cvt_f32_ubyte1_e32 v86, v30
	v_cvt_f32_ubyte2_e32 v87, v30
	v_cvt_f32_ubyte3_e32 v88, v30
	v_fmac_f32_e32 v10, v85, v54
	v_fmac_f32_e32 v11, v86, v54
	v_fmac_f32_e32 v12, v87, v54
	v_fmac_f32_e32 v13, v88, v54
	v_cvt_f32_ubyte0_e32 v85, v31
	v_cvt_f32_ubyte1_e32 v86, v31
	v_cvt_f32_ubyte2_e32 v87, v31
	v_cvt_f32_ubyte3_e32 v88, v31
	v_fmac_f32_e32 v14, v85, v54
	v_fmac_f32_e32 v15, v86, v54
	v_fmac_f32_e32 v16, v87, v54
	v_fmac_f32_e32 v17, v88, v54
	v_add_f32_e32 v18, v18, v54
	v_and_b32_e32 v84, 0xffff, v80
	v_lshl_or_b32 v83, v84, 7, v89
	global_load_dwordx4 v[28:31], v83, s[12:13]
	v_lshlrev_b32_e32 v109, 1, v84
	global_load_ushort v54, v109, s[14:15]
	s_waitcnt vmcnt(6)
	v_cvt_f32_f16_e32 v55, v55
	v_cvt_f32_ubyte0_e32 v85, v32
	v_cvt_f32_ubyte1_e32 v86, v32
	v_cvt_f32_ubyte2_e32 v87, v32
	v_cvt_f32_ubyte3_e32 v88, v32
	v_fmac_f32_e32 v2, v85, v55
	v_fmac_f32_e32 v3, v86, v55
	v_fmac_f32_e32 v4, v87, v55
	v_fmac_f32_e32 v5, v88, v55
	v_cvt_f32_ubyte0_e32 v85, v33
	v_cvt_f32_ubyte1_e32 v86, v33
	v_cvt_f32_ubyte2_e32 v87, v33
	v_cvt_f32_ubyte3_e32 v88, v33
	v_fmac_f32_e32 v6, v85, v55
	v_fmac_f32_e32 v7, v86, v55
	v_fmac_f32_e32 v8, v87, v55
	v_fmac_f32_e32 v9, v88, v55
	v_cvt_f32_ubyte0_e32 v85, v34
	v_cvt_f32_ubyte1_e32 v86, v34
	v_cvt_f32_ubyte2_e32 v87, v34
	v_cvt_f32_ubyte3_e32 v88, v34
	v_fmac_f32_e32 v10, v85, v55
	v_fmac_f32_e32 v11, v86, v55
	v_fmac_f32_e32 v12, v87, v55
	v_fmac_f32_e32 v13, v88, v55
	v_cvt_f32_ubyte0_e32 v85, v35
	v_cvt_f32_ubyte1_e32 v86, v35
	v_cvt_f32_ubyte2_e32 v87, v35
	v_cvt_f32_ubyte3_e32 v88, v35
	v_fmac_f32_e32 v14, v85, v55
	v_fmac_f32_e32 v15, v86, v55
	v_fmac_f32_e32 v16, v87, v55
	v_fmac_f32_e32 v17, v88, v55
	v_add_f32_e32 v18, v18, v55
	v_lshrrev_b32_e32 v84, 16, v80
	v_lshl_or_b32 v83, v84, 7, v89
	global_load_dwordx4 v[32:35], v83, s[12:13]
	v_lshlrev_b32_e32 v109, 1, v84
	global_load_ushort v55, v109, s[14:15]
	s_cmp_le_u32 s40, 16
	s_cbranch_scc1 .Lg1_tail0
	s_waitcnt lgkmcnt(0)
	ds_bpermute_b32 v80, v90, v74 offset:4
	s_waitcnt vmcnt(6)
	v_cvt_f32_f16_e32 v52, v52
	v_cvt_f32_ubyte0_e32 v85, v20
	v_cvt_f32_ubyte1_e32 v86, v20
	v_cvt_f32_ubyte2_e32 v87, v20
	v_cvt_f32_ubyte3_e32 v88, v20
	v_fmac_f32_e32 v2, v85, v52
	v_fmac_f32_e32 v3, v86, v52
	v_fmac_f32_e32 v4, v87, v52
	v_fmac_f32_e32 v5, v88, v52
	v_cvt_f32_ubyte0_e32 v85, v21
	v_cvt_f32_ubyte1_e32 v86, v21
	v_cvt_f32_ubyte2_e32 v87, v21
	v_cvt_f32_ubyte3_e32 v88, v21
	v_fmac_f32_e32 v6, v85, v52
	v_fmac_f32_e32 v7, v86, v52
	v_fmac_f32_e32 v8, v87, v52
	v_fmac_f32_e32 v9, v88, v52
	v_cvt_f32_ubyte0_e32 v85, v22
	v_cvt_f32_ubyte1_e32 v86, v22
	v_cvt_f32_ubyte2_e32 v87, v22
	v_cvt_f32_ubyte3_e32 v88, v22
	v_fmac_f32_e32 v10, v85, v52
	v_fmac_f32_e32 v11, v86, v52
	v_fmac_f32_e32 v12, v87, v52
	v_fmac_f32_e32 v13, v88, v52
	v_cvt_f32_ubyte0_e32 v85, v23
	v_cvt_f32_ubyte1_e32 v86, v23
	v_cvt_f32_ubyte2_e32 v87, v23
	v_cvt_f32_ubyte3_e32 v88, v23
	v_fmac_f32_e32 v14, v85, v52
	v_fmac_f32_e32 v15, v86, v52
	v_fmac_f32_e32 v16, v87, v52
	v_fmac_f32_e32 v17, v88, v52
	v_add_f32_e32 v18, v18, v52
	v_and_b32_e32 v84, 0xffff, v79
	v_lshl_or_b32 v83, v84, 7, v89
	global_load_dwordx4 v[20:23], v83, s[12:13]
	v_lshlrev_b32_e32 v109, 1, v84
	global_load_ushort v52, v109, s[14:15]
	s_waitcnt vmcnt(6)
	v_cvt_f32_f16_e32 v53, v53
	v_cvt_f32_ubyte0_e32 v85, v24
	v_cvt_f32_ubyte1_e32 v86, v24
	v_cvt_f32_ubyte2_e32 v87, v24
	v_cvt_f32_ubyte3_e32 v88, v24
	v_fmac_f32_e32 v2, v85, v53
	v_fmac_f32_e32 v3, v86, v53
	v_fmac_f32_e32 v4, v87, v53
	v_fmac_f32_e32 v5, v88, v53
	v_cvt_f32_ubyte0_e32 v85, v25
	v_cvt_f32_ubyte1_e32 v86, v25
	v_cvt_f32_ubyte2_e32 v87, v25
	v_cvt_f32_ubyte3_e32 v88, v25
	v_fmac_f32_e32 v6, v85, v53
	v_fmac_f32_e32 v7, v86, v53
	v_fmac_f32_e32 v8, v87, v53
	v_fmac_f32_e32 v9, v88, v53
	v_cvt_f32_ubyte0_e32 v85, v26
	v_cvt_f32_ubyte1_e32 v86, v26
	v_cvt_f32_ubyte2_e32 v87, v26
	v_cvt_f32_ubyte3_e32 v88, v26
	v_fmac_f32_e32 v10, v85, v53
	v_fmac_f32_e32 v11, v86, v53
	v_fmac_f32_e32 v12, v87, v53
	v_fmac_f32_e32 v13, v88, v53
	v_cvt_f32_ubyte0_e32 v85, v27
	v_cvt_f32_ubyte1_e32 v86, v27
	v_cvt_f32_ubyte2_e32 v87, v27
	v_cvt_f32_ubyte3_e32 v88, v27
	v_fmac_f32_e32 v14, v85, v53
	v_fmac_f32_e32 v15, v86, v53
	v_fmac_f32_e32 v16, v87, v53
	v_fmac_f32_e32 v17, v88, v53
	v_add_f32_e32 v18, v18, v53
	v_lshrrev_b32_e32 v84, 16, v79
	v_lshl_or_b32 v83, v84, 7, v89
	global_load_dwordx4 v[24:27], v83, s[12:13]
	v_lshlrev_b32_e32 v109, 1, v84
	global_load_ushort v53, v109, s[14:15]
	s_waitcnt lgkmcnt(0)
	ds_bpermute_b32 v79, v90, v74 offset:8
	s_waitcnt vmcnt(6)
	v_cvt_f32_f16_e32 v54, v54
	v_cvt_f32_ubyte0_e32 v85, v28
	v_cvt_f32_ubyte1_e32 v86, v28
	v_cvt_f32_ubyte2_e32 v87, v28
	v_cvt_f32_ubyte3_e32 v88, v28
	v_fmac_f32_e32 v2, v85, v54
	v_fmac_f32_e32 v3, v86, v54
	v_fmac_f32_e32 v4, v87, v54
	v_fmac_f32_e32 v5, v88, v54
	v_cvt_f32_ubyte0_e32 v85, v29
	v_cvt_f32_ubyte1_e32 v86, v29
	v_cvt_f32_ubyte2_e32 v87, v29
	v_cvt_f32_ubyte3_e32 v88, v29
	v_fmac_f32_e32 v6, v85, v54
	v_fmac_f32_e32 v7, v86, v54
	v_fmac_f32_e32 v8, v87, v54
	v_fmac_f32_e32 v9, v88, v54
	v_cvt_f32_ubyte0_e32 v85, v30
	v_cvt_f32_ubyte1_e32 v86, v30
	v_cvt_f32_ubyte2_e32 v87, v30
	v_cvt_f32_ubyte3_e32 v88, v30
	v_fmac_f32_e32 v10, v85, v54
	v_fmac_f32_e32 v11, v86, v54
	v_fmac_f32_e32 v12, v87, v54
	v_fmac_f32_e32 v13, v88, v54
	v_cvt_f32_ubyte0_e32 v85, v31
	v_cvt_f32_ubyte1_e32 v86, v31
	v_cvt_f32_ubyte2_e32 v87, v31
	v_cvt_f32_ubyte3_e32 v88, v31
	v_fmac_f32_e32 v14, v85, v54
	v_fmac_f32_e32 v15, v86, v54
	v_fmac_f32_e32 v16, v87, v54
	v_fmac_f32_e32 v17, v88, v54
	v_add_f32_e32 v18, v18, v54
	v_and_b32_e32 v84, 0xffff, v80
	v_lshl_or_b32 v83, v84, 7, v89
	global_load_dwordx4 v[28:31], v83, s[12:13]
	v_lshlrev_b32_e32 v109, 1, v84
	global_load_ushort v54, v109, s[14:15]
	s_waitcnt vmcnt(6)
	v_cvt_f32_f16_e32 v55, v55
	v_cvt_f32_ubyte0_e32 v85, v32
	v_cvt_f32_ubyte1_e32 v86, v32
	v_cvt_f32_ubyte2_e32 v87, v32
	v_cvt_f32_ubyte3_e32 v88, v32
	v_fmac_f32_e32 v2, v85, v55
	v_fmac_f32_e32 v3, v86, v55
	v_fmac_f32_e32 v4, v87, v55
	v_fmac_f32_e32 v5, v88, v55
	v_cvt_f32_ubyte0_e32 v85, v33
	v_cvt_f32_ubyte1_e32 v86, v33
	v_cvt_f32_ubyte2_e32 v87, v33
	v_cvt_f32_ubyte3_e32 v88, v33
	v_fmac_f32_e32 v6, v85, v55
	v_fmac_f32_e32 v7, v86, v55
	v_fmac_f32_e32 v8, v87, v55
	v_fmac_f32_e32 v9, v88, v55
	v_cvt_f32_ubyte0_e32 v85, v34
	v_cvt_f32_ubyte1_e32 v86, v34
	v_cvt_f32_ubyte2_e32 v87, v34
	v_cvt_f32_ubyte3_e32 v88, v34
	v_fmac_f32_e32 v10, v85, v55
	v_fmac_f32_e32 v11, v86, v55
	v_fmac_f32_e32 v12, v87, v55
	v_fmac_f32_e32 v13, v88, v55
	v_cvt_f32_ubyte0_e32 v85, v35
	v_cvt_f32_ubyte1_e32 v86, v35
	v_cvt_f32_ubyte2_e32 v87, v35
	v_cvt_f32_ubyte3_e32 v88, v35
	v_fmac_f32_e32 v14, v85, v55
	v_fmac_f32_e32 v15, v86, v55
	v_fmac_f32_e32 v16, v87, v55
	v_fmac_f32_e32 v17, v88, v55
	v_add_f32_e32 v18, v18, v55
	v_lshrrev_b32_e32 v84, 16, v80
	v_lshl_or_b32 v83, v84, 7, v89
	global_load_dwordx4 v[32:35], v83, s[12:13]
	v_lshlrev_b32_e32 v109, 1, v84
	global_load_ushort v55, v109, s[14:15]
	s_cmp_le_u32 s40, 20
	s_cbranch_scc1 .Lg1_tail0
	s_waitcnt lgkmcnt(0)
	ds_bpermute_b32 v80, v90, v74 offset:12
	s_waitcnt vmcnt(6)
	v_cvt_f32_f16_e32 v52, v52
	v_cvt_f32_ubyte0_e32 v85, v20
	v_cvt_f32_ubyte1_e32 v86, v20
	v_cvt_f32_ubyte2_e32 v87, v20
	v_cvt_f32_ubyte3_e32 v88, v20
	v_fmac_f32_e32 v2, v85, v52
	v_fmac_f32_e32 v3, v86, v52
	v_fmac_f32_e32 v4, v87, v52
	v_fmac_f32_e32 v5, v88, v52
	v_cvt_f32_ubyte0_e32 v85, v21
	v_cvt_f32_ubyte1_e32 v86, v21
	v_cvt_f32_ubyte2_e32 v87, v21
	v_cvt_f32_ubyte3_e32 v88, v21
	v_fmac_f32_e32 v6, v85, v52
	v_fmac_f32_e32 v7, v86, v52
	v_fmac_f32_e32 v8, v87, v52
	v_fmac_f32_e32 v9, v88, v52
	v_cvt_f32_ubyte0_e32 v85, v22
	v_cvt_f32_ubyte1_e32 v86, v22
	v_cvt_f32_ubyte2_e32 v87, v22
	v_cvt_f32_ubyte3_e32 v88, v22
	v_fmac_f32_e32 v10, v85, v52
	v_fmac_f32_e32 v11, v86, v52
	v_fmac_f32_e32 v12, v87, v52
	v_fmac_f32_e32 v13, v88, v52
	v_cvt_f32_ubyte0_e32 v85, v23
	v_cvt_f32_ubyte1_e32 v86, v23
	v_cvt_f32_ubyte2_e32 v87, v23
	v_cvt_f32_ubyte3_e32 v88, v23
	v_fmac_f32_e32 v14, v85, v52
	v_fmac_f32_e32 v15, v86, v52
	v_fmac_f32_e32 v16, v87, v52
	v_fmac_f32_e32 v17, v88, v52
	v_add_f32_e32 v18, v18, v52
	v_and_b32_e32 v84, 0xffff, v79
	v_lshl_or_b32 v83, v84, 7, v89
	global_load_dwordx4 v[20:23], v83, s[12:13]
	v_lshlrev_b32_e32 v109, 1, v84
	global_load_ushort v52, v109, s[14:15]
	s_waitcnt vmcnt(6)
	v_cvt_f32_f16_e32 v53, v53
	v_cvt_f32_ubyte0_e32 v85, v24
	v_cvt_f32_ubyte1_e32 v86, v24
	v_cvt_f32_ubyte2_e32 v87, v24
	v_cvt_f32_ubyte3_e32 v88, v24
	v_fmac_f32_e32 v2, v85, v53
	v_fmac_f32_e32 v3, v86, v53
	v_fmac_f32_e32 v4, v87, v53
	v_fmac_f32_e32 v5, v88, v53
	v_cvt_f32_ubyte0_e32 v85, v25
	v_cvt_f32_ubyte1_e32 v86, v25
	v_cvt_f32_ubyte2_e32 v87, v25
	v_cvt_f32_ubyte3_e32 v88, v25
	v_fmac_f32_e32 v6, v85, v53
	v_fmac_f32_e32 v7, v86, v53
	v_fmac_f32_e32 v8, v87, v53
	v_fmac_f32_e32 v9, v88, v53
	v_cvt_f32_ubyte0_e32 v85, v26
	v_cvt_f32_ubyte1_e32 v86, v26
	v_cvt_f32_ubyte2_e32 v87, v26
	v_cvt_f32_ubyte3_e32 v88, v26
	v_fmac_f32_e32 v10, v85, v53
	v_fmac_f32_e32 v11, v86, v53
	v_fmac_f32_e32 v12, v87, v53
	v_fmac_f32_e32 v13, v88, v53
	v_cvt_f32_ubyte0_e32 v85, v27
	v_cvt_f32_ubyte1_e32 v86, v27
	v_cvt_f32_ubyte2_e32 v87, v27
	v_cvt_f32_ubyte3_e32 v88, v27
	v_fmac_f32_e32 v14, v85, v53
	v_fmac_f32_e32 v15, v86, v53
	v_fmac_f32_e32 v16, v87, v53
	v_fmac_f32_e32 v17, v88, v53
	v_add_f32_e32 v18, v18, v53
	v_lshrrev_b32_e32 v84, 16, v79
	v_lshl_or_b32 v83, v84, 7, v89
	global_load_dwordx4 v[24:27], v83, s[12:13]
	v_lshlrev_b32_e32 v109, 1, v84
	global_load_ushort v53, v109, s[14:15]
	s_waitcnt lgkmcnt(0)
	ds_bpermute_b32 v79, v90, v74 offset:16
	s_waitcnt vmcnt(6)
	v_cvt_f32_f16_e32 v54, v54
	v_cvt_f32_ubyte0_e32 v85, v28
	v_cvt_f32_ubyte1_e32 v86, v28
	v_cvt_f32_ubyte2_e32 v87, v28
	v_cvt_f32_ubyte3_e32 v88, v28
	v_fmac_f32_e32 v2, v85, v54
	v_fmac_f32_e32 v3, v86, v54
	v_fmac_f32_e32 v4, v87, v54
	v_fmac_f32_e32 v5, v88, v54
	v_cvt_f32_ubyte0_e32 v85, v29
	v_cvt_f32_ubyte1_e32 v86, v29
	v_cvt_f32_ubyte2_e32 v87, v29
	v_cvt_f32_ubyte3_e32 v88, v29
	v_fmac_f32_e32 v6, v85, v54
	v_fmac_f32_e32 v7, v86, v54
	v_fmac_f32_e32 v8, v87, v54
	v_fmac_f32_e32 v9, v88, v54
	v_cvt_f32_ubyte0_e32 v85, v30
	v_cvt_f32_ubyte1_e32 v86, v30
	v_cvt_f32_ubyte2_e32 v87, v30
	v_cvt_f32_ubyte3_e32 v88, v30
	v_fmac_f32_e32 v10, v85, v54
	v_fmac_f32_e32 v11, v86, v54
	v_fmac_f32_e32 v12, v87, v54
	v_fmac_f32_e32 v13, v88, v54
	v_cvt_f32_ubyte0_e32 v85, v31
	v_cvt_f32_ubyte1_e32 v86, v31
	v_cvt_f32_ubyte2_e32 v87, v31
	v_cvt_f32_ubyte3_e32 v88, v31
	v_fmac_f32_e32 v14, v85, v54
	v_fmac_f32_e32 v15, v86, v54
	v_fmac_f32_e32 v16, v87, v54
	v_fmac_f32_e32 v17, v88, v54
	v_add_f32_e32 v18, v18, v54
	v_and_b32_e32 v84, 0xffff, v80
	v_lshl_or_b32 v83, v84, 7, v89
	global_load_dwordx4 v[28:31], v83, s[12:13]
	v_lshlrev_b32_e32 v109, 1, v84
	global_load_ushort v54, v109, s[14:15]
	s_waitcnt vmcnt(6)
	v_cvt_f32_f16_e32 v55, v55
	v_cvt_f32_ubyte0_e32 v85, v32
	v_cvt_f32_ubyte1_e32 v86, v32
	v_cvt_f32_ubyte2_e32 v87, v32
	v_cvt_f32_ubyte3_e32 v88, v32
	v_fmac_f32_e32 v2, v85, v55
	v_fmac_f32_e32 v3, v86, v55
	v_fmac_f32_e32 v4, v87, v55
	v_fmac_f32_e32 v5, v88, v55
	v_cvt_f32_ubyte0_e32 v85, v33
	v_cvt_f32_ubyte1_e32 v86, v33
	v_cvt_f32_ubyte2_e32 v87, v33
	v_cvt_f32_ubyte3_e32 v88, v33
	v_fmac_f32_e32 v6, v85, v55
	v_fmac_f32_e32 v7, v86, v55
	v_fmac_f32_e32 v8, v87, v55
	v_fmac_f32_e32 v9, v88, v55
	v_cvt_f32_ubyte0_e32 v85, v34
	v_cvt_f32_ubyte1_e32 v86, v34
	v_cvt_f32_ubyte2_e32 v87, v34
	v_cvt_f32_ubyte3_e32 v88, v34
	v_fmac_f32_e32 v10, v85, v55
	v_fmac_f32_e32 v11, v86, v55
	v_fmac_f32_e32 v12, v87, v55
	v_fmac_f32_e32 v13, v88, v55
	v_cvt_f32_ubyte0_e32 v85, v35
	v_cvt_f32_ubyte1_e32 v86, v35
	v_cvt_f32_ubyte2_e32 v87, v35
	v_cvt_f32_ubyte3_e32 v88, v35
	v_fmac_f32_e32 v14, v85, v55
	v_fmac_f32_e32 v15, v86, v55
	v_fmac_f32_e32 v16, v87, v55
	v_fmac_f32_e32 v17, v88, v55
	v_add_f32_e32 v18, v18, v55
	v_lshrrev_b32_e32 v84, 16, v80
	v_lshl_or_b32 v83, v84, 7, v89
	global_load_dwordx4 v[32:35], v83, s[12:13]
	v_lshlrev_b32_e32 v109, 1, v84
	global_load_ushort v55, v109, s[14:15]
	s_cmp_le_u32 s40, 24
	s_cbranch_scc1 .Lg1_tail0
	s_waitcnt lgkmcnt(0)
	ds_bpermute_b32 v80, v90, v74 offset:20
	s_waitcnt vmcnt(6)
	v_cvt_f32_f16_e32 v52, v52
	v_cvt_f32_ubyte0_e32 v85, v20
	v_cvt_f32_ubyte1_e32 v86, v20
	v_cvt_f32_ubyte2_e32 v87, v20
	v_cvt_f32_ubyte3_e32 v88, v20
	v_fmac_f32_e32 v2, v85, v52
	v_fmac_f32_e32 v3, v86, v52
	v_fmac_f32_e32 v4, v87, v52
	v_fmac_f32_e32 v5, v88, v52
	v_cvt_f32_ubyte0_e32 v85, v21
	v_cvt_f32_ubyte1_e32 v86, v21
	v_cvt_f32_ubyte2_e32 v87, v21
	v_cvt_f32_ubyte3_e32 v88, v21
	v_fmac_f32_e32 v6, v85, v52
	v_fmac_f32_e32 v7, v86, v52
	v_fmac_f32_e32 v8, v87, v52
	v_fmac_f32_e32 v9, v88, v52
	v_cvt_f32_ubyte0_e32 v85, v22
	v_cvt_f32_ubyte1_e32 v86, v22
	v_cvt_f32_ubyte2_e32 v87, v22
	v_cvt_f32_ubyte3_e32 v88, v22
	v_fmac_f32_e32 v10, v85, v52
	v_fmac_f32_e32 v11, v86, v52
	v_fmac_f32_e32 v12, v87, v52
	v_fmac_f32_e32 v13, v88, v52
	v_cvt_f32_ubyte0_e32 v85, v23
	v_cvt_f32_ubyte1_e32 v86, v23
	v_cvt_f32_ubyte2_e32 v87, v23
	v_cvt_f32_ubyte3_e32 v88, v23
	v_fmac_f32_e32 v14, v85, v52
	v_fmac_f32_e32 v15, v86, v52
	v_fmac_f32_e32 v16, v87, v52
	v_fmac_f32_e32 v17, v88, v52
	v_add_f32_e32 v18, v18, v52
	v_and_b32_e32 v84, 0xffff, v79
	v_lshl_or_b32 v83, v84, 7, v89
	global_load_dwordx4 v[20:23], v83, s[12:13]
	v_lshlrev_b32_e32 v109, 1, v84
	global_load_ushort v52, v109, s[14:15]
	s_waitcnt vmcnt(6)
	v_cvt_f32_f16_e32 v53, v53
	v_cvt_f32_ubyte0_e32 v85, v24
	v_cvt_f32_ubyte1_e32 v86, v24
	v_cvt_f32_ubyte2_e32 v87, v24
	v_cvt_f32_ubyte3_e32 v88, v24
	v_fmac_f32_e32 v2, v85, v53
	v_fmac_f32_e32 v3, v86, v53
	v_fmac_f32_e32 v4, v87, v53
	v_fmac_f32_e32 v5, v88, v53
	v_cvt_f32_ubyte0_e32 v85, v25
	v_cvt_f32_ubyte1_e32 v86, v25
	v_cvt_f32_ubyte2_e32 v87, v25
	v_cvt_f32_ubyte3_e32 v88, v25
	v_fmac_f32_e32 v6, v85, v53
	v_fmac_f32_e32 v7, v86, v53
	v_fmac_f32_e32 v8, v87, v53
	v_fmac_f32_e32 v9, v88, v53
	v_cvt_f32_ubyte0_e32 v85, v26
	v_cvt_f32_ubyte1_e32 v86, v26
	v_cvt_f32_ubyte2_e32 v87, v26
	v_cvt_f32_ubyte3_e32 v88, v26
	v_fmac_f32_e32 v10, v85, v53
	v_fmac_f32_e32 v11, v86, v53
	v_fmac_f32_e32 v12, v87, v53
	v_fmac_f32_e32 v13, v88, v53
	v_cvt_f32_ubyte0_e32 v85, v27
	v_cvt_f32_ubyte1_e32 v86, v27
	v_cvt_f32_ubyte2_e32 v87, v27
	v_cvt_f32_ubyte3_e32 v88, v27
	v_fmac_f32_e32 v14, v85, v53
	v_fmac_f32_e32 v15, v86, v53
	v_fmac_f32_e32 v16, v87, v53
	v_fmac_f32_e32 v17, v88, v53
	v_add_f32_e32 v18, v18, v53
	v_lshrrev_b32_e32 v84, 16, v79
	v_lshl_or_b32 v83, v84, 7, v89
	global_load_dwordx4 v[24:27], v83, s[12:13]
	v_lshlrev_b32_e32 v109, 1, v84
	global_load_ushort v53, v109, s[14:15]
	s_waitcnt lgkmcnt(0)
	ds_bpermute_b32 v79, v90, v74 offset:24
	s_waitcnt vmcnt(6)
	v_cvt_f32_f16_e32 v54, v54
	v_cvt_f32_ubyte0_e32 v85, v28
	v_cvt_f32_ubyte1_e32 v86, v28
	v_cvt_f32_ubyte2_e32 v87, v28
	v_cvt_f32_ubyte3_e32 v88, v28
	v_fmac_f32_e32 v2, v85, v54
	v_fmac_f32_e32 v3, v86, v54
	v_fmac_f32_e32 v4, v87, v54
	v_fmac_f32_e32 v5, v88, v54
	v_cvt_f32_ubyte0_e32 v85, v29
	v_cvt_f32_ubyte1_e32 v86, v29
	v_cvt_f32_ubyte2_e32 v87, v29
	v_cvt_f32_ubyte3_e32 v88, v29
	v_fmac_f32_e32 v6, v85, v54
	v_fmac_f32_e32 v7, v86, v54
	v_fmac_f32_e32 v8, v87, v54
	v_fmac_f32_e32 v9, v88, v54
	v_cvt_f32_ubyte0_e32 v85, v30
	v_cvt_f32_ubyte1_e32 v86, v30
	v_cvt_f32_ubyte2_e32 v87, v30
	v_cvt_f32_ubyte3_e32 v88, v30
	v_fmac_f32_e32 v10, v85, v54
	v_fmac_f32_e32 v11, v86, v54
	v_fmac_f32_e32 v12, v87, v54
	v_fmac_f32_e32 v13, v88, v54
	v_cvt_f32_ubyte0_e32 v85, v31
	v_cvt_f32_ubyte1_e32 v86, v31
	v_cvt_f32_ubyte2_e32 v87, v31
	v_cvt_f32_ubyte3_e32 v88, v31
	v_fmac_f32_e32 v14, v85, v54
	v_fmac_f32_e32 v15, v86, v54
	v_fmac_f32_e32 v16, v87, v54
	v_fmac_f32_e32 v17, v88, v54
	v_add_f32_e32 v18, v18, v54
	v_and_b32_e32 v84, 0xffff, v80
	v_lshl_or_b32 v83, v84, 7, v89
	global_load_dwordx4 v[28:31], v83, s[12:13]
	v_lshlrev_b32_e32 v109, 1, v84
	global_load_ushort v54, v109, s[14:15]
	s_waitcnt vmcnt(6)
	v_cvt_f32_f16_e32 v55, v55
	v_cvt_f32_ubyte0_e32 v85, v32
	v_cvt_f32_ubyte1_e32 v86, v32
	v_cvt_f32_ubyte2_e32 v87, v32
	v_cvt_f32_ubyte3_e32 v88, v32
	v_fmac_f32_e32 v2, v85, v55
	v_fmac_f32_e32 v3, v86, v55
	v_fmac_f32_e32 v4, v87, v55
	v_fmac_f32_e32 v5, v88, v55
	v_cvt_f32_ubyte0_e32 v85, v33
	v_cvt_f32_ubyte1_e32 v86, v33
	v_cvt_f32_ubyte2_e32 v87, v33
	v_cvt_f32_ubyte3_e32 v88, v33
	v_fmac_f32_e32 v6, v85, v55
	v_fmac_f32_e32 v7, v86, v55
	v_fmac_f32_e32 v8, v87, v55
	v_fmac_f32_e32 v9, v88, v55
	v_cvt_f32_ubyte0_e32 v85, v34
	v_cvt_f32_ubyte1_e32 v86, v34
	v_cvt_f32_ubyte2_e32 v87, v34
	v_cvt_f32_ubyte3_e32 v88, v34
	v_fmac_f32_e32 v10, v85, v55
	v_fmac_f32_e32 v11, v86, v55
	v_fmac_f32_e32 v12, v87, v55
	v_fmac_f32_e32 v13, v88, v55
	v_cvt_f32_ubyte0_e32 v85, v35
	v_cvt_f32_ubyte1_e32 v86, v35
	v_cvt_f32_ubyte2_e32 v87, v35
	v_cvt_f32_ubyte3_e32 v88, v35
	v_fmac_f32_e32 v14, v85, v55
	v_fmac_f32_e32 v15, v86, v55
	v_fmac_f32_e32 v16, v87, v55
	v_fmac_f32_e32 v17, v88, v55
	v_add_f32_e32 v18, v18, v55
	v_lshrrev_b32_e32 v84, 16, v80
	v_lshl_or_b32 v83, v84, 7, v89
	global_load_dwordx4 v[32:35], v83, s[12:13]
	v_lshlrev_b32_e32 v109, 1, v84
	global_load_ushort v55, v109, s[14:15]
	s_cmp_le_u32 s40, 28
	s_cbranch_scc1 .Lg1_tail0
	s_waitcnt lgkmcnt(0)
	ds_bpermute_b32 v80, v90, v74 offset:28
	s_waitcnt vmcnt(6)
	v_cvt_f32_f16_e32 v52, v52
	v_cvt_f32_ubyte0_e32 v85, v20
	v_cvt_f32_ubyte1_e32 v86, v20
	v_cvt_f32_ubyte2_e32 v87, v20
	v_cvt_f32_ubyte3_e32 v88, v20
	v_fmac_f32_e32 v2, v85, v52
	v_fmac_f32_e32 v3, v86, v52
	v_fmac_f32_e32 v4, v87, v52
	v_fmac_f32_e32 v5, v88, v52
	v_cvt_f32_ubyte0_e32 v85, v21
	v_cvt_f32_ubyte1_e32 v86, v21
	v_cvt_f32_ubyte2_e32 v87, v21
	v_cvt_f32_ubyte3_e32 v88, v21
	v_fmac_f32_e32 v6, v85, v52
	v_fmac_f32_e32 v7, v86, v52
	v_fmac_f32_e32 v8, v87, v52
	v_fmac_f32_e32 v9, v88, v52
	v_cvt_f32_ubyte0_e32 v85, v22
	v_cvt_f32_ubyte1_e32 v86, v22
	v_cvt_f32_ubyte2_e32 v87, v22
	v_cvt_f32_ubyte3_e32 v88, v22
	v_fmac_f32_e32 v10, v85, v52
	v_fmac_f32_e32 v11, v86, v52
	v_fmac_f32_e32 v12, v87, v52
	v_fmac_f32_e32 v13, v88, v52
	v_cvt_f32_ubyte0_e32 v85, v23
	v_cvt_f32_ubyte1_e32 v86, v23
	v_cvt_f32_ubyte2_e32 v87, v23
	v_cvt_f32_ubyte3_e32 v88, v23
	v_fmac_f32_e32 v14, v85, v52
	v_fmac_f32_e32 v15, v86, v52
	v_fmac_f32_e32 v16, v87, v52
	v_fmac_f32_e32 v17, v88, v52
	v_add_f32_e32 v18, v18, v52
	v_and_b32_e32 v84, 0xffff, v79
	v_lshl_or_b32 v83, v84, 7, v89
	global_load_dwordx4 v[20:23], v83, s[12:13]
	v_lshlrev_b32_e32 v109, 1, v84
	global_load_ushort v52, v109, s[14:15]
	s_waitcnt vmcnt(6)
	v_cvt_f32_f16_e32 v53, v53
	v_cvt_f32_ubyte0_e32 v85, v24
	v_cvt_f32_ubyte1_e32 v86, v24
	v_cvt_f32_ubyte2_e32 v87, v24
	v_cvt_f32_ubyte3_e32 v88, v24
	v_fmac_f32_e32 v2, v85, v53
	v_fmac_f32_e32 v3, v86, v53
	v_fmac_f32_e32 v4, v87, v53
	v_fmac_f32_e32 v5, v88, v53
	v_cvt_f32_ubyte0_e32 v85, v25
	v_cvt_f32_ubyte1_e32 v86, v25
	v_cvt_f32_ubyte2_e32 v87, v25
	v_cvt_f32_ubyte3_e32 v88, v25
	v_fmac_f32_e32 v6, v85, v53
	v_fmac_f32_e32 v7, v86, v53
	v_fmac_f32_e32 v8, v87, v53
	v_fmac_f32_e32 v9, v88, v53
	v_cvt_f32_ubyte0_e32 v85, v26
	v_cvt_f32_ubyte1_e32 v86, v26
	v_cvt_f32_ubyte2_e32 v87, v26
	v_cvt_f32_ubyte3_e32 v88, v26
	v_fmac_f32_e32 v10, v85, v53
	v_fmac_f32_e32 v11, v86, v53
	v_fmac_f32_e32 v12, v87, v53
	v_fmac_f32_e32 v13, v88, v53
	v_cvt_f32_ubyte0_e32 v85, v27
	v_cvt_f32_ubyte1_e32 v86, v27
	v_cvt_f32_ubyte2_e32 v87, v27
	v_cvt_f32_ubyte3_e32 v88, v27
	v_fmac_f32_e32 v14, v85, v53
	v_fmac_f32_e32 v15, v86, v53
	v_fmac_f32_e32 v16, v87, v53
	v_fmac_f32_e32 v17, v88, v53
	v_add_f32_e32 v18, v18, v53
	v_lshrrev_b32_e32 v84, 16, v79
	v_lshl_or_b32 v83, v84, 7, v89
	global_load_dwordx4 v[24:27], v83, s[12:13]
	v_lshlrev_b32_e32 v109, 1, v84
	global_load_ushort v53, v109, s[14:15]
	s_waitcnt lgkmcnt(0)
	s_waitcnt vmcnt(6)
	v_cvt_f32_f16_e32 v54, v54
	v_cvt_f32_ubyte0_e32 v85, v28
	v_cvt_f32_ubyte1_e32 v86, v28
	v_cvt_f32_ubyte2_e32 v87, v28
	v_cvt_f32_ubyte3_e32 v88, v28
	v_fmac_f32_e32 v2, v85, v54
	v_fmac_f32_e32 v3, v86, v54
	v_fmac_f32_e32 v4, v87, v54
	v_fmac_f32_e32 v5, v88, v54
	v_cvt_f32_ubyte0_e32 v85, v29
	v_cvt_f32_ubyte1_e32 v86, v29
	v_cvt_f32_ubyte2_e32 v87, v29
	v_cvt_f32_ubyte3_e32 v88, v29
	v_fmac_f32_e32 v6, v85, v54
	v_fmac_f32_e32 v7, v86, v54
	v_fmac_f32_e32 v8, v87, v54
	v_fmac_f32_e32 v9, v88, v54
	v_cvt_f32_ubyte0_e32 v85, v30
	v_cvt_f32_ubyte1_e32 v86, v30
	v_cvt_f32_ubyte2_e32 v87, v30
	v_cvt_f32_ubyte3_e32 v88, v30
	v_fmac_f32_e32 v10, v85, v54
	v_fmac_f32_e32 v11, v86, v54
	v_fmac_f32_e32 v12, v87, v54
	v_fmac_f32_e32 v13, v88, v54
	v_cvt_f32_ubyte0_e32 v85, v31
	v_cvt_f32_ubyte1_e32 v86, v31
	v_cvt_f32_ubyte2_e32 v87, v31
	v_cvt_f32_ubyte3_e32 v88, v31
	v_fmac_f32_e32 v14, v85, v54
	v_fmac_f32_e32 v15, v86, v54
	v_fmac_f32_e32 v16, v87, v54
	v_fmac_f32_e32 v17, v88, v54
	v_add_f32_e32 v18, v18, v54
	v_and_b32_e32 v84, 0xffff, v80
	v_lshl_or_b32 v83, v84, 7, v89
	global_load_dwordx4 v[28:31], v83, s[12:13]
	v_lshlrev_b32_e32 v109, 1, v84
	global_load_ushort v54, v109, s[14:15]
	s_waitcnt vmcnt(6)
	v_cvt_f32_f16_e32 v55, v55
	v_cvt_f32_ubyte0_e32 v85, v32
	v_cvt_f32_ubyte1_e32 v86, v32
	v_cvt_f32_ubyte2_e32 v87, v32
	v_cvt_f32_ubyte3_e32 v88, v32
	v_fmac_f32_e32 v2, v85, v55
	v_fmac_f32_e32 v3, v86, v55
	v_fmac_f32_e32 v4, v87, v55
	v_fmac_f32_e32 v5, v88, v55
	v_cvt_f32_ubyte0_e32 v85, v33
	v_cvt_f32_ubyte1_e32 v86, v33
	v_cvt_f32_ubyte2_e32 v87, v33
	v_cvt_f32_ubyte3_e32 v88, v33
	v_fmac_f32_e32 v6, v85, v55
	v_fmac_f32_e32 v7, v86, v55
	v_fmac_f32_e32 v8, v87, v55
	v_fmac_f32_e32 v9, v88, v55
	v_cvt_f32_ubyte0_e32 v85, v34
	v_cvt_f32_ubyte1_e32 v86, v34
	v_cvt_f32_ubyte2_e32 v87, v34
	v_cvt_f32_ubyte3_e32 v88, v34
	v_fmac_f32_e32 v10, v85, v55
	v_fmac_f32_e32 v11, v86, v55
	v_fmac_f32_e32 v12, v87, v55
	v_fmac_f32_e32 v13, v88, v55
	v_cvt_f32_ubyte0_e32 v85, v35
	v_cvt_f32_ubyte1_e32 v86, v35
	v_cvt_f32_ubyte2_e32 v87, v35
	v_cvt_f32_ubyte3_e32 v88, v35
	v_fmac_f32_e32 v14, v85, v55
	v_fmac_f32_e32 v15, v86, v55
	v_fmac_f32_e32 v16, v87, v55
	v_fmac_f32_e32 v17, v88, v55
	v_add_f32_e32 v18, v18, v55
	v_lshrrev_b32_e32 v84, 16, v80
	v_lshl_or_b32 v83, v84, 7, v89
	global_load_dwordx4 v[32:35], v83, s[12:13]
	v_lshlrev_b32_e32 v109, 1, v84
	global_load_ushort v55, v109, s[14:15]

.Lg2_active:
	s_mov_b32 s46, 0x01010101
	s_mov_b32 s47, 0x01010101
	s_mov_b32 s60, 0x00ff00ff
	s_mov_b32 s61, 0x0c030c01
	v_lshrrev_b32_e32 v107, 3, v1
	v_and_b32_e32 v108, 7, v1
	v_and_b32_e32 v105, 15, v1
	v_lshrrev_b32_e32 v106, 4, v1
	s_bfe_u32 s36, s3, 0x10002
	s_lshl_b32 s58, s36, 3
	s_xor_b32 s59, s58, 8
	v_or_b32_e32 v102, s58, v107
	v_or_b32_e32 v103, s59, v107
	v_lshlrev_b32_e32 v89, 4, v108
	v_and_b32_e32 v90, 56, v1
	v_lshlrev_b32_e32 v90, 2, v90
	s_waitcnt lgkmcnt(0)
	s_lshl_b32 s58, s6, 8
	s_add_u32 s32, s16, s58
	s_addc_u32 s33, s17, 0
	s_lshl_b32 s58, s6, 10
	s_add_u32 s34, s18, s58
	s_addc_u32 s35, s19, 0
	v_lshlrev_b32_e32 v109, 4, v105
	global_load_dword v104, v109, s[32:33] offset:8
	v_lshlrev_b32_e32 v110, 4, v102
	global_load_dwordx2 v[68:69], v110, s[32:33]
	v_lshlrev_b32_e32 v111, 4, v103
	global_load_dwordx2 v[70:71], v111, s[32:33]
	v_lshlrev_b32_e32 v101, 2, v108
	v_lshl_or_b32 v110, v102, 6, v101
	global_load_dword v60, v110, s[34:35]
	global_load_dword v61, v110, s[34:35] offset:32
	v_lshl_or_b32 v111, v103, 6, v101
	global_load_dword v62, v111, s[34:35]
	global_load_dword v63, v111, s[34:35] offset:32
	global_load_dwordx4 v[2:5], v95, s[22:23]
	global_load_dwordx4 v[6:9], v98, s[22:23]
	global_load_dwordx4 v[10:13], v99, s[22:23]
	global_load_dwordx4 v[14:17], v100, s[22:23]
	v_and_b32_e32 v101, 0x7f, v0
	v_lshlrev_b32_e32 v101, 2, v101
	global_load_dword v19, v101, s[24:25]
	s_mul_i32 s48, s3, 0x1100
	s_add_u32 s48, s48, 66048
	v_mul_u32_u24_e32 v91, 0x110, v102
	v_lshl_add_u32 v91, v108, 5, v91
	v_add_u32_e32 v91, s48, v91
	v_mul_u32_u24_e32 v92, 0x110, v103
	v_lshl_add_u32 v92, v108, 5, v92
	v_add_u32_e32 v92, s48, v92
	s_waitcnt vmcnt(5)
	v_readlane_b32 s49, v69, 0
	v_readlane_b32 s50, v69, 8
	v_readlane_b32 s51, v69, 16
	v_readlane_b32 s52, v69, 24
	v_readlane_b32 s53, v69, 32
	v_readlane_b32 s54, v69, 40
	v_readlane_b32 s55, v69, 48
	v_readlane_b32 s56, v69, 56
	s_max_i32 s37, s49, s50
	s_max_i32 s37, s37, s51
	s_max_i32 s37, s37, s52
	s_max_i32 s37, s37, s53
	s_max_i32 s37, s37, s54
	s_max_i32 s37, s37, s55
	s_max_i32 s37, s37, s56
	v_readlane_b32 s49, v71, 0
	v_readlane_b32 s50, v71, 8
	v_readlane_b32 s51, v71, 16
	v_readlane_b32 s52, v71, 24
	v_readlane_b32 s53, v71, 32
	v_readlane_b32 s54, v71, 40
	v_readlane_b32 s55, v71, 48
	v_readlane_b32 s56, v71, 56
	s_max_i32 s38, s49, s50
	s_max_i32 s38, s38, s51
	s_max_i32 s38, s38, s52
	s_max_i32 s38, s38, s53
	s_max_i32 s38, s38, s54
	s_max_i32 s38, s38, s55
	s_max_i32 s38, s38, s56
	v_lshlrev_b32_e32 v103, 8, v104
	v_lshl_or_b32 v103, v106, 4, v103
	s_waitcnt vmcnt(0)
	ds_write_b128 v96, v[2:5]
	ds_write_b128 v96, v[6:9] offset:16384
	ds_write_b128 v96, v[10:13] offset:32768
	ds_write_b128 v96, v[14:17] offset:49152
	v_add_u32_e32 v101, 0x10000, v101
	ds_write_b32 v101, v19
	s_waitcnt lgkmcnt(0)
	s_barrier
	s_mov_b32 s39, 0

.Lg2_sel_done:
	s_min_i32 s40, s41, 32
	s_add_i32 s40, s40, 3
	s_and_b32 s40, s40, 0x3c
	s_max_i32 s40, s40, 4
	v_mov_b32_e32 v2, 0
	v_mov_b32_e32 v3, 0
	v_mov_b32_e32 v4, 0
	v_mov_b32_e32 v5, 0
	v_mov_b32_e32 v6, 0
	v_mov_b32_e32 v7, 0
	v_mov_b32_e32 v8, 0
	v_mov_b32_e32 v9, 0
	v_mov_b32_e32 v10, 0
	v_mov_b32_e32 v11, 0
	v_mov_b32_e32 v12, 0
	v_mov_b32_e32 v13, 0
	v_mov_b32_e32 v14, 0
	v_mov_b32_e32 v15, 0
	v_mov_b32_e32 v16, 0
	v_mov_b32_e32 v17, 0
	s_waitcnt lgkmcnt(0)
	ds_bpermute_b32 v94, v90, v73 offset:0
	ds_bpermute_b32 v95, v90, v73 offset:4
	ds_bpermute_b32 v79, v90, v73 offset:8
	s_waitcnt lgkmcnt(1)
	v_and_b32_e32 v84, 0xffff, v94
	v_lshl_or_b32 v83, v84, 7, v89
	global_load_dwordx4 v[20:23], v83, s[12:13]
	v_lshlrev_b32_e32 v109, 1, v84
	global_load_ushort v52, v109, s[14:15]
	v_lshrrev_b32_e32 v84, 16, v94
	v_lshl_or_b32 v83, v84, 7, v89
	global_load_dwordx4 v[24:27], v83, s[12:13]
	v_lshlrev_b32_e32 v109, 1, v84
	global_load_ushort v53, v109, s[14:15]
	v_and_b32_e32 v84, 0xffff, v95
	v_lshl_or_b32 v83, v84, 7, v89
	global_load_dwordx4 v[28:31], v83, s[12:13]
	v_lshlrev_b32_e32 v109, 1, v84
	global_load_ushort v54, v109, s[14:15]
	v_lshrrev_b32_e32 v84, 16, v95
	v_lshl_or_b32 v83, v84, 7, v89
	global_load_dwordx4 v[32:35], v83, s[12:13]
	v_lshlrev_b32_e32 v109, 1, v84
	global_load_ushort v55, v109, s[14:15]
	s_cmp_le_u32 s40, 4
	s_cbranch_scc1 .Lg2_tail0
	s_waitcnt lgkmcnt(0)
	ds_bpermute_b32 v80, v90, v73 offset:12
	s_waitcnt vmcnt(6)
	v_cvt_f32_f16_e32 v52, v52
	v_cvt_f32_ubyte0_e32 v85, v20
	v_cvt_f32_ubyte1_e32 v86, v20
	v_cvt_f32_ubyte2_e32 v87, v20
	v_cvt_f32_ubyte3_e32 v88, v20
	v_fmac_f32_e32 v2, v85, v52
	v_fmac_f32_e32 v3, v86, v52
	v_fmac_f32_e32 v4, v87, v52
	v_fmac_f32_e32 v5, v88, v52
	v_cvt_f32_ubyte0_e32 v85, v21
	v_cvt_f32_ubyte1_e32 v86, v21
	v_cvt_f32_ubyte2_e32 v87, v21
	v_cvt_f32_ubyte3_e32 v88, v21
	v_fmac_f32_e32 v6, v85, v52
	v_fmac_f32_e32 v7, v86, v52
	v_fmac_f32_e32 v8, v87, v52
	v_fmac_f32_e32 v9, v88, v52
	v_cvt_f32_ubyte0_e32 v85, v22
	v_cvt_f32_ubyte1_e32 v86, v22
	v_cvt_f32_ubyte2_e32 v87, v22
	v_cvt_f32_ubyte3_e32 v88, v22
	v_fmac_f32_e32 v10, v85, v52
	v_fmac_f32_e32 v11, v86, v52
	v_fmac_f32_e32 v12, v87, v52
	v_fmac_f32_e32 v13, v88, v52
	v_cvt_f32_ubyte0_e32 v85, v23
	v_cvt_f32_ubyte1_e32 v86, v23
	v_cvt_f32_ubyte2_e32 v87, v23
	v_cvt_f32_ubyte3_e32 v88, v23
	v_fmac_f32_e32 v14, v85, v52
	v_fmac_f32_e32 v15, v86, v52
	v_fmac_f32_e32 v16, v87, v52
	v_fmac_f32_e32 v17, v88, v52
	v_and_b32_e32 v84, 0xffff, v79
	v_lshl_or_b32 v83, v84, 7, v89
	global_load_dwordx4 v[20:23], v83, s[12:13]
	v_lshlrev_b32_e32 v109, 1, v84
	global_load_ushort v52, v109, s[14:15]
	s_waitcnt vmcnt(6)
	v_cvt_f32_f16_e32 v53, v53
	v_cvt_f32_ubyte0_e32 v85, v24
	v_cvt_f32_ubyte1_e32 v86, v24
	v_cvt_f32_ubyte2_e32 v87, v24
	v_cvt_f32_ubyte3_e32 v88, v24
	v_fmac_f32_e32 v2, v85, v53
	v_fmac_f32_e32 v3, v86, v53
	v_fmac_f32_e32 v4, v87, v53
	v_fmac_f32_e32 v5, v88, v53
	v_cvt_f32_ubyte0_e32 v85, v25
	v_cvt_f32_ubyte1_e32 v86, v25
	v_cvt_f32_ubyte2_e32 v87, v25
	v_cvt_f32_ubyte3_e32 v88, v25
	v_fmac_f32_e32 v6, v85, v53
	v_fmac_f32_e32 v7, v86, v53
	v_fmac_f32_e32 v8, v87, v53
	v_fmac_f32_e32 v9, v88, v53
	v_cvt_f32_ubyte0_e32 v85, v26
	v_cvt_f32_ubyte1_e32 v86, v26
	v_cvt_f32_ubyte2_e32 v87, v26
	v_cvt_f32_ubyte3_e32 v88, v26
	v_fmac_f32_e32 v10, v85, v53
	v_fmac_f32_e32 v11, v86, v53
	v_fmac_f32_e32 v12, v87, v53
	v_fmac_f32_e32 v13, v88, v53
	v_cvt_f32_ubyte0_e32 v85, v27
	v_cvt_f32_ubyte1_e32 v86, v27
	v_cvt_f32_ubyte2_e32 v87, v27
	v_cvt_f32_ubyte3_e32 v88, v27
	v_fmac_f32_e32 v14, v85, v53
	v_fmac_f32_e32 v15, v86, v53
	v_fmac_f32_e32 v16, v87, v53
	v_fmac_f32_e32 v17, v88, v53
	v_lshrrev_b32_e32 v84, 16, v79
	v_lshl_or_b32 v83, v84, 7, v89
	global_load_dwordx4 v[24:27], v83, s[12:13]
	v_lshlrev_b32_e32 v109, 1, v84
	global_load_ushort v53, v109, s[14:15]
	s_waitcnt lgkmcnt(0)
	ds_bpermute_b32 v79, v90, v73 offset:16
	s_waitcnt vmcnt(6)
	v_cvt_f32_f16_e32 v54, v54
	v_cvt_f32_ubyte0_e32 v85, v28
	v_cvt_f32_ubyte1_e32 v86, v28
	v_cvt_f32_ubyte2_e32 v87, v28
	v_cvt_f32_ubyte3_e32 v88, v28
	v_fmac_f32_e32 v2, v85, v54
	v_fmac_f32_e32 v3, v86, v54
	v_fmac_f32_e32 v4, v87, v54
	v_fmac_f32_e32 v5, v88, v54
	v_cvt_f32_ubyte0_e32 v85, v29
	v_cvt_f32_ubyte1_e32 v86, v29
	v_cvt_f32_ubyte2_e32 v87, v29
	v_cvt_f32_ubyte3_e32 v88, v29
	v_fmac_f32_e32 v6, v85, v54
	v_fmac_f32_e32 v7, v86, v54
	v_fmac_f32_e32 v8, v87, v54
	v_fmac_f32_e32 v9, v88, v54
	v_cvt_f32_ubyte0_e32 v85, v30
	v_cvt_f32_ubyte1_e32 v86, v30
	v_cvt_f32_ubyte2_e32 v87, v30
	v_cvt_f32_ubyte3_e32 v88, v30
	v_fmac_f32_e32 v10, v85, v54
	v_fmac_f32_e32 v11, v86, v54
	v_fmac_f32_e32 v12, v87, v54
	v_fmac_f32_e32 v13, v88, v54
	v_cvt_f32_ubyte0_e32 v85, v31
	v_cvt_f32_ubyte1_e32 v86, v31
	v_cvt_f32_ubyte2_e32 v87, v31
	v_cvt_f32_ubyte3_e32 v88, v31
	v_fmac_f32_e32 v14, v85, v54
	v_fmac_f32_e32 v15, v86, v54
	v_fmac_f32_e32 v16, v87, v54
	v_fmac_f32_e32 v17, v88, v54
	v_and_b32_e32 v84, 0xffff, v80
	v_lshl_or_b32 v83, v84, 7, v89
	global_load_dwordx4 v[28:31], v83, s[12:13]
	v_lshlrev_b32_e32 v109, 1, v84
	global_load_ushort v54, v109, s[14:15]
	s_waitcnt vmcnt(6)
	v_cvt_f32_f16_e32 v55, v55
	v_cvt_f32_ubyte0_e32 v85, v32
	v_cvt_f32_ubyte1_e32 v86, v32
	v_cvt_f32_ubyte2_e32 v87, v32
	v_cvt_f32_ubyte3_e32 v88, v32
	v_fmac_f32_e32 v2, v85, v55
	v_fmac_f32_e32 v3, v86, v55
	v_fmac_f32_e32 v4, v87, v55
	v_fmac_f32_e32 v5, v88, v55
	v_cvt_f32_ubyte0_e32 v85, v33
	v_cvt_f32_ubyte1_e32 v86, v33
	v_cvt_f32_ubyte2_e32 v87, v33
	v_cvt_f32_ubyte3_e32 v88, v33
	v_fmac_f32_e32 v6, v85, v55
	v_fmac_f32_e32 v7, v86, v55
	v_fmac_f32_e32 v8, v87, v55
	v_fmac_f32_e32 v9, v88, v55
	v_cvt_f32_ubyte0_e32 v85, v34
	v_cvt_f32_ubyte1_e32 v86, v34
	v_cvt_f32_ubyte2_e32 v87, v34
	v_cvt_f32_ubyte3_e32 v88, v34
	v_fmac_f32_e32 v10, v85, v55
	v_fmac_f32_e32 v11, v86, v55
	v_fmac_f32_e32 v12, v87, v55
	v_fmac_f32_e32 v13, v88, v55
	v_cvt_f32_ubyte0_e32 v85, v35
	v_cvt_f32_ubyte1_e32 v86, v35
	v_cvt_f32_ubyte2_e32 v87, v35
	v_cvt_f32_ubyte3_e32 v88, v35
	v_fmac_f32_e32 v14, v85, v55
	v_fmac_f32_e32 v15, v86, v55
	v_fmac_f32_e32 v16, v87, v55
	v_fmac_f32_e32 v17, v88, v55
	v_lshrrev_b32_e32 v84, 16, v80
	v_lshl_or_b32 v83, v84, 7, v89
	global_load_dwordx4 v[32:35], v83, s[12:13]
	v_lshlrev_b32_e32 v109, 1, v84
	global_load_ushort v55, v109, s[14:15]
	s_cmp_le_u32 s40, 8
	s_cbranch_scc1 .Lg2_tail0
	s_waitcnt lgkmcnt(0)
	ds_bpermute_b32 v80, v90, v73 offset:20
	s_waitcnt vmcnt(6)
	v_cvt_f32_f16_e32 v52, v52
	v_cvt_f32_ubyte0_e32 v85, v20
	v_cvt_f32_ubyte1_e32 v86, v20
	v_cvt_f32_ubyte2_e32 v87, v20
	v_cvt_f32_ubyte3_e32 v88, v20
	v_fmac_f32_e32 v2, v85, v52
	v_fmac_f32_e32 v3, v86, v52
	v_fmac_f32_e32 v4, v87, v52
	v_fmac_f32_e32 v5, v88, v52
	v_cvt_f32_ubyte0_e32 v85, v21
	v_cvt_f32_ubyte1_e32 v86, v21
	v_cvt_f32_ubyte2_e32 v87, v21
	v_cvt_f32_ubyte3_e32 v88, v21
	v_fmac_f32_e32 v6, v85, v52
	v_fmac_f32_e32 v7, v86, v52
	v_fmac_f32_e32 v8, v87, v52
	v_fmac_f32_e32 v9, v88, v52
	v_cvt_f32_ubyte0_e32 v85, v22
	v_cvt_f32_ubyte1_e32 v86, v22
	v_cvt_f32_ubyte2_e32 v87, v22
	v_cvt_f32_ubyte3_e32 v88, v22
	v_fmac_f32_e32 v10, v85, v52
	v_fmac_f32_e32 v11, v86, v52
	v_fmac_f32_e32 v12, v87, v52
	v_fmac_f32_e32 v13, v88, v52
	v_cvt_f32_ubyte0_e32 v85, v23
	v_cvt_f32_ubyte1_e32 v86, v23
	v_cvt_f32_ubyte2_e32 v87, v23
	v_cvt_f32_ubyte3_e32 v88, v23
	v_fmac_f32_e32 v14, v85, v52
	v_fmac_f32_e32 v15, v86, v52
	v_fmac_f32_e32 v16, v87, v52
	v_fmac_f32_e32 v17, v88, v52
	v_and_b32_e32 v84, 0xffff, v79
	v_lshl_or_b32 v83, v84, 7, v89
	global_load_dwordx4 v[20:23], v83, s[12:13]
	v_lshlrev_b32_e32 v109, 1, v84
	global_load_ushort v52, v109, s[14:15]
	s_waitcnt vmcnt(6)
	v_cvt_f32_f16_e32 v53, v53
	v_cvt_f32_ubyte0_e32 v85, v24
	v_cvt_f32_ubyte1_e32 v86, v24
	v_cvt_f32_ubyte2_e32 v87, v24
	v_cvt_f32_ubyte3_e32 v88, v24
	v_fmac_f32_e32 v2, v85, v53
	v_fmac_f32_e32 v3, v86, v53
	v_fmac_f32_e32 v4, v87, v53
	v_fmac_f32_e32 v5, v88, v53
	v_cvt_f32_ubyte0_e32 v85, v25
	v_cvt_f32_ubyte1_e32 v86, v25
	v_cvt_f32_ubyte2_e32 v87, v25
	v_cvt_f32_ubyte3_e32 v88, v25
	v_fmac_f32_e32 v6, v85, v53
	v_fmac_f32_e32 v7, v86, v53
	v_fmac_f32_e32 v8, v87, v53
	v_fmac_f32_e32 v9, v88, v53
	v_cvt_f32_ubyte0_e32 v85, v26
	v_cvt_f32_ubyte1_e32 v86, v26
	v_cvt_f32_ubyte2_e32 v87, v26
	v_cvt_f32_ubyte3_e32 v88, v26
	v_fmac_f32_e32 v10, v85, v53
	v_fmac_f32_e32 v11, v86, v53
	v_fmac_f32_e32 v12, v87, v53
	v_fmac_f32_e32 v13, v88, v53
	v_cvt_f32_ubyte0_e32 v85, v27
	v_cvt_f32_ubyte1_e32 v86, v27
	v_cvt_f32_ubyte2_e32 v87, v27
	v_cvt_f32_ubyte3_e32 v88, v27
	v_fmac_f32_e32 v14, v85, v53
	v_fmac_f32_e32 v15, v86, v53
	v_fmac_f32_e32 v16, v87, v53
	v_fmac_f32_e32 v17, v88, v53
	v_lshrrev_b32_e32 v84, 16, v79
	v_lshl_or_b32 v83, v84, 7, v89
	global_load_dwordx4 v[24:27], v83, s[12:13]
	v_lshlrev_b32_e32 v109, 1, v84
	global_load_ushort v53, v109, s[14:15]
	s_waitcnt lgkmcnt(0)
	ds_bpermute_b32 v79, v90, v73 offset:24
	s_waitcnt vmcnt(6)
	v_cvt_f32_f16_e32 v54, v54
	v_cvt_f32_ubyte0_e32 v85, v28
	v_cvt_f32_ubyte1_e32 v86, v28
	v_cvt_f32_ubyte2_e32 v87, v28
	v_cvt_f32_ubyte3_e32 v88, v28
	v_fmac_f32_e32 v2, v85, v54
	v_fmac_f32_e32 v3, v86, v54
	v_fmac_f32_e32 v4, v87, v54
	v_fmac_f32_e32 v5, v88, v54
	v_cvt_f32_ubyte0_e32 v85, v29
	v_cvt_f32_ubyte1_e32 v86, v29
	v_cvt_f32_ubyte2_e32 v87, v29
	v_cvt_f32_ubyte3_e32 v88, v29
	v_fmac_f32_e32 v6, v85, v54
	v_fmac_f32_e32 v7, v86, v54
	v_fmac_f32_e32 v8, v87, v54
	v_fmac_f32_e32 v9, v88, v54
	v_cvt_f32_ubyte0_e32 v85, v30
	v_cvt_f32_ubyte1_e32 v86, v30
	v_cvt_f32_ubyte2_e32 v87, v30
	v_cvt_f32_ubyte3_e32 v88, v30
	v_fmac_f32_e32 v10, v85, v54
	v_fmac_f32_e32 v11, v86, v54
	v_fmac_f32_e32 v12, v87, v54
	v_fmac_f32_e32 v13, v88, v54
	v_cvt_f32_ubyte0_e32 v85, v31
	v_cvt_f32_ubyte1_e32 v86, v31
	v_cvt_f32_ubyte2_e32 v87, v31
	v_cvt_f32_ubyte3_e32 v88, v31
	v_fmac_f32_e32 v14, v85, v54
	v_fmac_f32_e32 v15, v86, v54
	v_fmac_f32_e32 v16, v87, v54
	v_fmac_f32_e32 v17, v88, v54
	v_and_b32_e32 v84, 0xffff, v80
	v_lshl_or_b32 v83, v84, 7, v89
	global_load_dwordx4 v[28:31], v83, s[12:13]
	v_lshlrev_b32_e32 v109, 1, v84
	global_load_ushort v54, v109, s[14:15]
	s_waitcnt vmcnt(6)
	v_cvt_f32_f16_e32 v55, v55
	v_cvt_f32_ubyte0_e32 v85, v32
	v_cvt_f32_ubyte1_e32 v86, v32
	v_cvt_f32_ubyte2_e32 v87, v32
	v_cvt_f32_ubyte3_e32 v88, v32
	v_fmac_f32_e32 v2, v85, v55
	v_fmac_f32_e32 v3, v86, v55
	v_fmac_f32_e32 v4, v87, v55
	v_fmac_f32_e32 v5, v88, v55
	v_cvt_f32_ubyte0_e32 v85, v33
	v_cvt_f32_ubyte1_e32 v86, v33
	v_cvt_f32_ubyte2_e32 v87, v33
	v_cvt_f32_ubyte3_e32 v88, v33
	v_fmac_f32_e32 v6, v85, v55
	v_fmac_f32_e32 v7, v86, v55
	v_fmac_f32_e32 v8, v87, v55
	v_fmac_f32_e32 v9, v88, v55
	v_cvt_f32_ubyte0_e32 v85, v34
	v_cvt_f32_ubyte1_e32 v86, v34
	v_cvt_f32_ubyte2_e32 v87, v34
	v_cvt_f32_ubyte3_e32 v88, v34
	v_fmac_f32_e32 v10, v85, v55
	v_fmac_f32_e32 v11, v86, v55
	v_fmac_f32_e32 v12, v87, v55
	v_fmac_f32_e32 v13, v88, v55
	v_cvt_f32_ubyte0_e32 v85, v35
	v_cvt_f32_ubyte1_e32 v86, v35
	v_cvt_f32_ubyte2_e32 v87, v35
	v_cvt_f32_ubyte3_e32 v88, v35
	v_fmac_f32_e32 v14, v85, v55
	v_fmac_f32_e32 v15, v86, v55
	v_fmac_f32_e32 v16, v87, v55
	v_fmac_f32_e32 v17, v88, v55
	v_lshrrev_b32_e32 v84, 16, v80
	v_lshl_or_b32 v83, v84, 7, v89
	global_load_dwordx4 v[32:35], v83, s[12:13]
	v_lshlrev_b32_e32 v109, 1, v84
	global_load_ushort v55, v109, s[14:15]
	s_cmp_le_u32 s40, 12
	s_cbranch_scc1 .Lg2_tail0
	s_waitcnt lgkmcnt(0)
	ds_bpermute_b32 v80, v90, v73 offset:28
	s_waitcnt vmcnt(6)
	v_cvt_f32_f16_e32 v52, v52
	v_cvt_f32_ubyte0_e32 v85, v20
	v_cvt_f32_ubyte1_e32 v86, v20
	v_cvt_f32_ubyte2_e32 v87, v20
	v_cvt_f32_ubyte3_e32 v88, v20
	v_fmac_f32_e32 v2, v85, v52
	v_fmac_f32_e32 v3, v86, v52
	v_fmac_f32_e32 v4, v87, v52
	v_fmac_f32_e32 v5, v88, v52
	v_cvt_f32_ubyte0_e32 v85, v21
	v_cvt_f32_ubyte1_e32 v86, v21
	v_cvt_f32_ubyte2_e32 v87, v21
	v_cvt_f32_ubyte3_e32 v88, v21
	v_fmac_f32_e32 v6, v85, v52
	v_fmac_f32_e32 v7, v86, v52
	v_fmac_f32_e32 v8, v87, v52
	v_fmac_f32_e32 v9, v88, v52
	v_cvt_f32_ubyte0_e32 v85, v22
	v_cvt_f32_ubyte1_e32 v86, v22
	v_cvt_f32_ubyte2_e32 v87, v22
	v_cvt_f32_ubyte3_e32 v88, v22
	v_fmac_f32_e32 v10, v85, v52
	v_fmac_f32_e32 v11, v86, v52
	v_fmac_f32_e32 v12, v87, v52
	v_fmac_f32_e32 v13, v88, v52
	v_cvt_f32_ubyte0_e32 v85, v23
	v_cvt_f32_ubyte1_e32 v86, v23
	v_cvt_f32_ubyte2_e32 v87, v23
	v_cvt_f32_ubyte3_e32 v88, v23
	v_fmac_f32_e32 v14, v85, v52
	v_fmac_f32_e32 v15, v86, v52
	v_fmac_f32_e32 v16, v87, v52
	v_fmac_f32_e32 v17, v88, v52
	v_and_b32_e32 v84, 0xffff, v79
	v_lshl_or_b32 v83, v84, 7, v89
	global_load_dwordx4 v[20:23], v83, s[12:13]
	v_lshlrev_b32_e32 v109, 1, v84
	global_load_ushort v52, v109, s[14:15]
	s_waitcnt vmcnt(6)
	v_cvt_f32_f16_e32 v53, v53
	v_cvt_f32_ubyte0_e32 v85, v24
	v_cvt_f32_ubyte1_e32 v86, v24
	v_cvt_f32_ubyte2_e32 v87, v24
	v_cvt_f32_ubyte3_e32 v88, v24
	v_fmac_f32_e32 v2, v85, v53
	v_fmac_f32_e32 v3, v86, v53
	v_fmac_f32_e32 v4, v87, v53
	v_fmac_f32_e32 v5, v88, v53
	v_cvt_f32_ubyte0_e32 v85, v25
	v_cvt_f32_ubyte1_e32 v86, v25
	v_cvt_f32_ubyte2_e32 v87, v25
	v_cvt_f32_ubyte3_e32 v88, v25
	v_fmac_f32_e32 v6, v85, v53
	v_fmac_f32_e32 v7, v86, v53
	v_fmac_f32_e32 v8, v87, v53
	v_fmac_f32_e32 v9, v88, v53
	v_cvt_f32_ubyte0_e32 v85, v26
	v_cvt_f32_ubyte1_e32 v86, v26
	v_cvt_f32_ubyte2_e32 v87, v26
	v_cvt_f32_ubyte3_e32 v88, v26
	v_fmac_f32_e32 v10, v85, v53
	v_fmac_f32_e32 v11, v86, v53
	v_fmac_f32_e32 v12, v87, v53
	v_fmac_f32_e32 v13, v88, v53
	v_cvt_f32_ubyte0_e32 v85, v27
	v_cvt_f32_ubyte1_e32 v86, v27
	v_cvt_f32_ubyte2_e32 v87, v27
	v_cvt_f32_ubyte3_e32 v88, v27
	v_fmac_f32_e32 v14, v85, v53
	v_fmac_f32_e32 v15, v86, v53
	v_fmac_f32_e32 v16, v87, v53
	v_fmac_f32_e32 v17, v88, v53
	v_lshrrev_b32_e32 v84, 16, v79
	v_lshl_or_b32 v83, v84, 7, v89
	global_load_dwordx4 v[24:27], v83, s[12:13]
	v_lshlrev_b32_e32 v109, 1, v84
	global_load_ushort v53, v109, s[14:15]
	s_waitcnt lgkmcnt(0)
	ds_bpermute_b32 v79, v90, v74 offset:0
	s_waitcnt vmcnt(6)
	v_cvt_f32_f16_e32 v54, v54
	v_cvt_f32_ubyte0_e32 v85, v28
	v_cvt_f32_ubyte1_e32 v86, v28
	v_cvt_f32_ubyte2_e32 v87, v28
	v_cvt_f32_ubyte3_e32 v88, v28
	v_fmac_f32_e32 v2, v85, v54
	v_fmac_f32_e32 v3, v86, v54
	v_fmac_f32_e32 v4, v87, v54
	v_fmac_f32_e32 v5, v88, v54
	v_cvt_f32_ubyte0_e32 v85, v29
	v_cvt_f32_ubyte1_e32 v86, v29
	v_cvt_f32_ubyte2_e32 v87, v29
	v_cvt_f32_ubyte3_e32 v88, v29
	v_fmac_f32_e32 v6, v85, v54
	v_fmac_f32_e32 v7, v86, v54
	v_fmac_f32_e32 v8, v87, v54
	v_fmac_f32_e32 v9, v88, v54
	v_cvt_f32_ubyte0_e32 v85, v30
	v_cvt_f32_ubyte1_e32 v86, v30
	v_cvt_f32_ubyte2_e32 v87, v30
	v_cvt_f32_ubyte3_e32 v88, v30
	v_fmac_f32_e32 v10, v85, v54
	v_fmac_f32_e32 v11, v86, v54
	v_fmac_f32_e32 v12, v87, v54
	v_fmac_f32_e32 v13, v88, v54
	v_cvt_f32_ubyte0_e32 v85, v31
	v_cvt_f32_ubyte1_e32 v86, v31
	v_cvt_f32_ubyte2_e32 v87, v31
	v_cvt_f32_ubyte3_e32 v88, v31
	v_fmac_f32_e32 v14, v85, v54
	v_fmac_f32_e32 v15, v86, v54
	v_fmac_f32_e32 v16, v87, v54
	v_fmac_f32_e32 v17, v88, v54
	v_and_b32_e32 v84, 0xffff, v80
	v_lshl_or_b32 v83, v84, 7, v89
	global_load_dwordx4 v[28:31], v83, s[12:13]
	v_lshlrev_b32_e32 v109, 1, v84
	global_load_ushort v54, v109, s[14:15]
	s_waitcnt vmcnt(6)
	v_cvt_f32_f16_e32 v55, v55
	v_cvt_f32_ubyte0_e32 v85, v32
	v_cvt_f32_ubyte1_e32 v86, v32
	v_cvt_f32_ubyte2_e32 v87, v32
	v_cvt_f32_ubyte3_e32 v88, v32
	v_fmac_f32_e32 v2, v85, v55
	v_fmac_f32_e32 v3, v86, v55
	v_fmac_f32_e32 v4, v87, v55
	v_fmac_f32_e32 v5, v88, v55
	v_cvt_f32_ubyte0_e32 v85, v33
	v_cvt_f32_ubyte1_e32 v86, v33
	v_cvt_f32_ubyte2_e32 v87, v33
	v_cvt_f32_ubyte3_e32 v88, v33
	v_fmac_f32_e32 v6, v85, v55
	v_fmac_f32_e32 v7, v86, v55
	v_fmac_f32_e32 v8, v87, v55
	v_fmac_f32_e32 v9, v88, v55
	v_cvt_f32_ubyte0_e32 v85, v34
	v_cvt_f32_ubyte1_e32 v86, v34
	v_cvt_f32_ubyte2_e32 v87, v34
	v_cvt_f32_ubyte3_e32 v88, v34
	v_fmac_f32_e32 v10, v85, v55
	v_fmac_f32_e32 v11, v86, v55
	v_fmac_f32_e32 v12, v87, v55
	v_fmac_f32_e32 v13, v88, v55
	v_cvt_f32_ubyte0_e32 v85, v35
	v_cvt_f32_ubyte1_e32 v86, v35
	v_cvt_f32_ubyte2_e32 v87, v35
	v_cvt_f32_ubyte3_e32 v88, v35
	v_fmac_f32_e32 v14, v85, v55
	v_fmac_f32_e32 v15, v86, v55
	v_fmac_f32_e32 v16, v87, v55
	v_fmac_f32_e32 v17, v88, v55
	v_lshrrev_b32_e32 v84, 16, v80
	v_lshl_or_b32 v83, v84, 7, v89
	global_load_dwordx4 v[32:35], v83, s[12:13]
	v_lshlrev_b32_e32 v109, 1, v84
	global_load_ushort v55, v109, s[14:15]
	s_cmp_le_u32 s40, 16
	s_cbranch_scc1 .Lg2_tail0
	s_waitcnt lgkmcnt(0)
	ds_bpermute_b32 v80, v90, v74 offset:4
	s_waitcnt vmcnt(6)
	v_cvt_f32_f16_e32 v52, v52
	v_cvt_f32_ubyte0_e32 v85, v20
	v_cvt_f32_ubyte1_e32 v86, v20
	v_cvt_f32_ubyte2_e32 v87, v20
	v_cvt_f32_ubyte3_e32 v88, v20
	v_fmac_f32_e32 v2, v85, v52
	v_fmac_f32_e32 v3, v86, v52
	v_fmac_f32_e32 v4, v87, v52
	v_fmac_f32_e32 v5, v88, v52
	v_cvt_f32_ubyte0_e32 v85, v21
	v_cvt_f32_ubyte1_e32 v86, v21
	v_cvt_f32_ubyte2_e32 v87, v21
	v_cvt_f32_ubyte3_e32 v88, v21
	v_fmac_f32_e32 v6, v85, v52
	v_fmac_f32_e32 v7, v86, v52
	v_fmac_f32_e32 v8, v87, v52
	v_fmac_f32_e32 v9, v88, v52
	v_cvt_f32_ubyte0_e32 v85, v22
	v_cvt_f32_ubyte1_e32 v86, v22
	v_cvt_f32_ubyte2_e32 v87, v22
	v_cvt_f32_ubyte3_e32 v88, v22
	v_fmac_f32_e32 v10, v85, v52
	v_fmac_f32_e32 v11, v86, v52
	v_fmac_f32_e32 v12, v87, v52
	v_fmac_f32_e32 v13, v88, v52
	v_cvt_f32_ubyte0_e32 v85, v23
	v_cvt_f32_ubyte1_e32 v86, v23
	v_cvt_f32_ubyte2_e32 v87, v23
	v_cvt_f32_ubyte3_e32 v88, v23
	v_fmac_f32_e32 v14, v85, v52
	v_fmac_f32_e32 v15, v86, v52
	v_fmac_f32_e32 v16, v87, v52
	v_fmac_f32_e32 v17, v88, v52
	v_and_b32_e32 v84, 0xffff, v79
	v_lshl_or_b32 v83, v84, 7, v89
	global_load_dwordx4 v[20:23], v83, s[12:13]
	v_lshlrev_b32_e32 v109, 1, v84
	global_load_ushort v52, v109, s[14:15]
	s_waitcnt vmcnt(6)
	v_cvt_f32_f16_e32 v53, v53
	v_cvt_f32_ubyte0_e32 v85, v24
	v_cvt_f32_ubyte1_e32 v86, v24
	v_cvt_f32_ubyte2_e32 v87, v24
	v_cvt_f32_ubyte3_e32 v88, v24
	v_fmac_f32_e32 v2, v85, v53
	v_fmac_f32_e32 v3, v86, v53
	v_fmac_f32_e32 v4, v87, v53
	v_fmac_f32_e32 v5, v88, v53
	v_cvt_f32_ubyte0_e32 v85, v25
	v_cvt_f32_ubyte1_e32 v86, v25
	v_cvt_f32_ubyte2_e32 v87, v25
	v_cvt_f32_ubyte3_e32 v88, v25
	v_fmac_f32_e32 v6, v85, v53
	v_fmac_f32_e32 v7, v86, v53
	v_fmac_f32_e32 v8, v87, v53
	v_fmac_f32_e32 v9, v88, v53
	v_cvt_f32_ubyte0_e32 v85, v26
	v_cvt_f32_ubyte1_e32 v86, v26
	v_cvt_f32_ubyte2_e32 v87, v26
	v_cvt_f32_ubyte3_e32 v88, v26
	v_fmac_f32_e32 v10, v85, v53
	v_fmac_f32_e32 v11, v86, v53
	v_fmac_f32_e32 v12, v87, v53
	v_fmac_f32_e32 v13, v88, v53
	v_cvt_f32_ubyte0_e32 v85, v27
	v_cvt_f32_ubyte1_e32 v86, v27
	v_cvt_f32_ubyte2_e32 v87, v27
	v_cvt_f32_ubyte3_e32 v88, v27
	v_fmac_f32_e32 v14, v85, v53
	v_fmac_f32_e32 v15, v86, v53
	v_fmac_f32_e32 v16, v87, v53
	v_fmac_f32_e32 v17, v88, v53
	v_lshrrev_b32_e32 v84, 16, v79
	v_lshl_or_b32 v83, v84, 7, v89
	global_load_dwordx4 v[24:27], v83, s[12:13]
	v_lshlrev_b32_e32 v109, 1, v84
	global_load_ushort v53, v109, s[14:15]
	s_waitcnt lgkmcnt(0)
	ds_bpermute_b32 v79, v90, v74 offset:8
	s_waitcnt vmcnt(6)
	v_cvt_f32_f16_e32 v54, v54
	v_cvt_f32_ubyte0_e32 v85, v28
	v_cvt_f32_ubyte1_e32 v86, v28
	v_cvt_f32_ubyte2_e32 v87, v28
	v_cvt_f32_ubyte3_e32 v88, v28
	v_fmac_f32_e32 v2, v85, v54
	v_fmac_f32_e32 v3, v86, v54
	v_fmac_f32_e32 v4, v87, v54
	v_fmac_f32_e32 v5, v88, v54
	v_cvt_f32_ubyte0_e32 v85, v29
	v_cvt_f32_ubyte1_e32 v86, v29
	v_cvt_f32_ubyte2_e32 v87, v29
	v_cvt_f32_ubyte3_e32 v88, v29
	v_fmac_f32_e32 v6, v85, v54
	v_fmac_f32_e32 v7, v86, v54
	v_fmac_f32_e32 v8, v87, v54
	v_fmac_f32_e32 v9, v88, v54
	v_cvt_f32_ubyte0_e32 v85, v30
	v_cvt_f32_ubyte1_e32 v86, v30
	v_cvt_f32_ubyte2_e32 v87, v30
	v_cvt_f32_ubyte3_e32 v88, v30
	v_fmac_f32_e32 v10, v85, v54
	v_fmac_f32_e32 v11, v86, v54
	v_fmac_f32_e32 v12, v87, v54
	v_fmac_f32_e32 v13, v88, v54
	v_cvt_f32_ubyte0_e32 v85, v31
	v_cvt_f32_ubyte1_e32 v86, v31
	v_cvt_f32_ubyte2_e32 v87, v31
	v_cvt_f32_ubyte3_e32 v88, v31
	v_fmac_f32_e32 v14, v85, v54
	v_fmac_f32_e32 v15, v86, v54
	v_fmac_f32_e32 v16, v87, v54
	v_fmac_f32_e32 v17, v88, v54
	v_and_b32_e32 v84, 0xffff, v80
	v_lshl_or_b32 v83, v84, 7, v89
	global_load_dwordx4 v[28:31], v83, s[12:13]
	v_lshlrev_b32_e32 v109, 1, v84
	global_load_ushort v54, v109, s[14:15]
	s_waitcnt vmcnt(6)
	v_cvt_f32_f16_e32 v55, v55
	v_cvt_f32_ubyte0_e32 v85, v32
	v_cvt_f32_ubyte1_e32 v86, v32
	v_cvt_f32_ubyte2_e32 v87, v32
	v_cvt_f32_ubyte3_e32 v88, v32
	v_fmac_f32_e32 v2, v85, v55
	v_fmac_f32_e32 v3, v86, v55
	v_fmac_f32_e32 v4, v87, v55
	v_fmac_f32_e32 v5, v88, v55
	v_cvt_f32_ubyte0_e32 v85, v33
	v_cvt_f32_ubyte1_e32 v86, v33
	v_cvt_f32_ubyte2_e32 v87, v33
	v_cvt_f32_ubyte3_e32 v88, v33
	v_fmac_f32_e32 v6, v85, v55
	v_fmac_f32_e32 v7, v86, v55
	v_fmac_f32_e32 v8, v87, v55
	v_fmac_f32_e32 v9, v88, v55
	v_cvt_f32_ubyte0_e32 v85, v34
	v_cvt_f32_ubyte1_e32 v86, v34
	v_cvt_f32_ubyte2_e32 v87, v34
	v_cvt_f32_ubyte3_e32 v88, v34
	v_fmac_f32_e32 v10, v85, v55
	v_fmac_f32_e32 v11, v86, v55
	v_fmac_f32_e32 v12, v87, v55
	v_fmac_f32_e32 v13, v88, v55
	v_cvt_f32_ubyte0_e32 v85, v35
	v_cvt_f32_ubyte1_e32 v86, v35
	v_cvt_f32_ubyte2_e32 v87, v35
	v_cvt_f32_ubyte3_e32 v88, v35
	v_fmac_f32_e32 v14, v85, v55
	v_fmac_f32_e32 v15, v86, v55
	v_fmac_f32_e32 v16, v87, v55
	v_fmac_f32_e32 v17, v88, v55
	v_lshrrev_b32_e32 v84, 16, v80
	v_lshl_or_b32 v83, v84, 7, v89
	global_load_dwordx4 v[32:35], v83, s[12:13]
	v_lshlrev_b32_e32 v109, 1, v84
	global_load_ushort v55, v109, s[14:15]
	s_cmp_le_u32 s40, 20
	s_cbranch_scc1 .Lg2_tail0
	s_waitcnt lgkmcnt(0)
	ds_bpermute_b32 v80, v90, v74 offset:12
	s_waitcnt vmcnt(6)
	v_cvt_f32_f16_e32 v52, v52
	v_cvt_f32_ubyte0_e32 v85, v20
	v_cvt_f32_ubyte1_e32 v86, v20
	v_cvt_f32_ubyte2_e32 v87, v20
	v_cvt_f32_ubyte3_e32 v88, v20
	v_fmac_f32_e32 v2, v85, v52
	v_fmac_f32_e32 v3, v86, v52
	v_fmac_f32_e32 v4, v87, v52
	v_fmac_f32_e32 v5, v88, v52
	v_cvt_f32_ubyte0_e32 v85, v21
	v_cvt_f32_ubyte1_e32 v86, v21
	v_cvt_f32_ubyte2_e32 v87, v21
	v_cvt_f32_ubyte3_e32 v88, v21
	v_fmac_f32_e32 v6, v85, v52
	v_fmac_f32_e32 v7, v86, v52
	v_fmac_f32_e32 v8, v87, v52
	v_fmac_f32_e32 v9, v88, v52
	v_cvt_f32_ubyte0_e32 v85, v22
	v_cvt_f32_ubyte1_e32 v86, v22
	v_cvt_f32_ubyte2_e32 v87, v22
	v_cvt_f32_ubyte3_e32 v88, v22
	v_fmac_f32_e32 v10, v85, v52
	v_fmac_f32_e32 v11, v86, v52
	v_fmac_f32_e32 v12, v87, v52
	v_fmac_f32_e32 v13, v88, v52
	v_cvt_f32_ubyte0_e32 v85, v23
	v_cvt_f32_ubyte1_e32 v86, v23
	v_cvt_f32_ubyte2_e32 v87, v23
	v_cvt_f32_ubyte3_e32 v88, v23
	v_fmac_f32_e32 v14, v85, v52
	v_fmac_f32_e32 v15, v86, v52
	v_fmac_f32_e32 v16, v87, v52
	v_fmac_f32_e32 v17, v88, v52
	v_and_b32_e32 v84, 0xffff, v79
	v_lshl_or_b32 v83, v84, 7, v89
	global_load_dwordx4 v[20:23], v83, s[12:13]
	v_lshlrev_b32_e32 v109, 1, v84
	global_load_ushort v52, v109, s[14:15]
	s_waitcnt vmcnt(6)
	v_cvt_f32_f16_e32 v53, v53
	v_cvt_f32_ubyte0_e32 v85, v24
	v_cvt_f32_ubyte1_e32 v86, v24
	v_cvt_f32_ubyte2_e32 v87, v24
	v_cvt_f32_ubyte3_e32 v88, v24
	v_fmac_f32_e32 v2, v85, v53
	v_fmac_f32_e32 v3, v86, v53
	v_fmac_f32_e32 v4, v87, v53
	v_fmac_f32_e32 v5, v88, v53
	v_cvt_f32_ubyte0_e32 v85, v25
	v_cvt_f32_ubyte1_e32 v86, v25
	v_cvt_f32_ubyte2_e32 v87, v25
	v_cvt_f32_ubyte3_e32 v88, v25
	v_fmac_f32_e32 v6, v85, v53
	v_fmac_f32_e32 v7, v86, v53
	v_fmac_f32_e32 v8, v87, v53
	v_fmac_f32_e32 v9, v88, v53
	v_cvt_f32_ubyte0_e32 v85, v26
	v_cvt_f32_ubyte1_e32 v86, v26
	v_cvt_f32_ubyte2_e32 v87, v26
	v_cvt_f32_ubyte3_e32 v88, v26
	v_fmac_f32_e32 v10, v85, v53
	v_fmac_f32_e32 v11, v86, v53
	v_fmac_f32_e32 v12, v87, v53
	v_fmac_f32_e32 v13, v88, v53
	v_cvt_f32_ubyte0_e32 v85, v27
	v_cvt_f32_ubyte1_e32 v86, v27
	v_cvt_f32_ubyte2_e32 v87, v27
	v_cvt_f32_ubyte3_e32 v88, v27
	v_fmac_f32_e32 v14, v85, v53
	v_fmac_f32_e32 v15, v86, v53
	v_fmac_f32_e32 v16, v87, v53
	v_fmac_f32_e32 v17, v88, v53
	v_lshrrev_b32_e32 v84, 16, v79
	v_lshl_or_b32 v83, v84, 7, v89
	global_load_dwordx4 v[24:27], v83, s[12:13]
	v_lshlrev_b32_e32 v109, 1, v84
	global_load_ushort v53, v109, s[14:15]
	s_waitcnt lgkmcnt(0)
	ds_bpermute_b32 v79, v90, v74 offset:16
	s_waitcnt vmcnt(6)
	v_cvt_f32_f16_e32 v54, v54
	v_cvt_f32_ubyte0_e32 v85, v28
	v_cvt_f32_ubyte1_e32 v86, v28
	v_cvt_f32_ubyte2_e32 v87, v28
	v_cvt_f32_ubyte3_e32 v88, v28
	v_fmac_f32_e32 v2, v85, v54
	v_fmac_f32_e32 v3, v86, v54
	v_fmac_f32_e32 v4, v87, v54
	v_fmac_f32_e32 v5, v88, v54
	v_cvt_f32_ubyte0_e32 v85, v29
	v_cvt_f32_ubyte1_e32 v86, v29
	v_cvt_f32_ubyte2_e32 v87, v29
	v_cvt_f32_ubyte3_e32 v88, v29
	v_fmac_f32_e32 v6, v85, v54
	v_fmac_f32_e32 v7, v86, v54
	v_fmac_f32_e32 v8, v87, v54
	v_fmac_f32_e32 v9, v88, v54
	v_cvt_f32_ubyte0_e32 v85, v30
	v_cvt_f32_ubyte1_e32 v86, v30
	v_cvt_f32_ubyte2_e32 v87, v30
	v_cvt_f32_ubyte3_e32 v88, v30
	v_fmac_f32_e32 v10, v85, v54
	v_fmac_f32_e32 v11, v86, v54
	v_fmac_f32_e32 v12, v87, v54
	v_fmac_f32_e32 v13, v88, v54
	v_cvt_f32_ubyte0_e32 v85, v31
	v_cvt_f32_ubyte1_e32 v86, v31
	v_cvt_f32_ubyte2_e32 v87, v31
	v_cvt_f32_ubyte3_e32 v88, v31
	v_fmac_f32_e32 v14, v85, v54
	v_fmac_f32_e32 v15, v86, v54
	v_fmac_f32_e32 v16, v87, v54
	v_fmac_f32_e32 v17, v88, v54
	v_and_b32_e32 v84, 0xffff, v80
	v_lshl_or_b32 v83, v84, 7, v89
	global_load_dwordx4 v[28:31], v83, s[12:13]
	v_lshlrev_b32_e32 v109, 1, v84
	global_load_ushort v54, v109, s[14:15]
	s_waitcnt vmcnt(6)
	v_cvt_f32_f16_e32 v55, v55
	v_cvt_f32_ubyte0_e32 v85, v32
	v_cvt_f32_ubyte1_e32 v86, v32
	v_cvt_f32_ubyte2_e32 v87, v32
	v_cvt_f32_ubyte3_e32 v88, v32
	v_fmac_f32_e32 v2, v85, v55
	v_fmac_f32_e32 v3, v86, v55
	v_fmac_f32_e32 v4, v87, v55
	v_fmac_f32_e32 v5, v88, v55
	v_cvt_f32_ubyte0_e32 v85, v33
	v_cvt_f32_ubyte1_e32 v86, v33
	v_cvt_f32_ubyte2_e32 v87, v33
	v_cvt_f32_ubyte3_e32 v88, v33
	v_fmac_f32_e32 v6, v85, v55
	v_fmac_f32_e32 v7, v86, v55
	v_fmac_f32_e32 v8, v87, v55
	v_fmac_f32_e32 v9, v88, v55
	v_cvt_f32_ubyte0_e32 v85, v34
	v_cvt_f32_ubyte1_e32 v86, v34
	v_cvt_f32_ubyte2_e32 v87, v34
	v_cvt_f32_ubyte3_e32 v88, v34
	v_fmac_f32_e32 v10, v85, v55
	v_fmac_f32_e32 v11, v86, v55
	v_fmac_f32_e32 v12, v87, v55
	v_fmac_f32_e32 v13, v88, v55
	v_cvt_f32_ubyte0_e32 v85, v35
	v_cvt_f32_ubyte1_e32 v86, v35
	v_cvt_f32_ubyte2_e32 v87, v35
	v_cvt_f32_ubyte3_e32 v88, v35
	v_fmac_f32_e32 v14, v85, v55
	v_fmac_f32_e32 v15, v86, v55
	v_fmac_f32_e32 v16, v87, v55
	v_fmac_f32_e32 v17, v88, v55
	v_lshrrev_b32_e32 v84, 16, v80
	v_lshl_or_b32 v83, v84, 7, v89
	global_load_dwordx4 v[32:35], v83, s[12:13]
	v_lshlrev_b32_e32 v109, 1, v84
	global_load_ushort v55, v109, s[14:15]
	s_cmp_le_u32 s40, 24
	s_cbranch_scc1 .Lg2_tail0
	s_waitcnt lgkmcnt(0)
	ds_bpermute_b32 v80, v90, v74 offset:20
	s_waitcnt vmcnt(6)
	v_cvt_f32_f16_e32 v52, v52
	v_cvt_f32_ubyte0_e32 v85, v20
	v_cvt_f32_ubyte1_e32 v86, v20
	v_cvt_f32_ubyte2_e32 v87, v20
	v_cvt_f32_ubyte3_e32 v88, v20
	v_fmac_f32_e32 v2, v85, v52
	v_fmac_f32_e32 v3, v86, v52
	v_fmac_f32_e32 v4, v87, v52
	v_fmac_f32_e32 v5, v88, v52
	v_cvt_f32_ubyte0_e32 v85, v21
	v_cvt_f32_ubyte1_e32 v86, v21
	v_cvt_f32_ubyte2_e32 v87, v21
	v_cvt_f32_ubyte3_e32 v88, v21
	v_fmac_f32_e32 v6, v85, v52
	v_fmac_f32_e32 v7, v86, v52
	v_fmac_f32_e32 v8, v87, v52
	v_fmac_f32_e32 v9, v88, v52
	v_cvt_f32_ubyte0_e32 v85, v22
	v_cvt_f32_ubyte1_e32 v86, v22
	v_cvt_f32_ubyte2_e32 v87, v22
	v_cvt_f32_ubyte3_e32 v88, v22
	v_fmac_f32_e32 v10, v85, v52
	v_fmac_f32_e32 v11, v86, v52
	v_fmac_f32_e32 v12, v87, v52
	v_fmac_f32_e32 v13, v88, v52
	v_cvt_f32_ubyte0_e32 v85, v23
	v_cvt_f32_ubyte1_e32 v86, v23
	v_cvt_f32_ubyte2_e32 v87, v23
	v_cvt_f32_ubyte3_e32 v88, v23
	v_fmac_f32_e32 v14, v85, v52
	v_fmac_f32_e32 v15, v86, v52
	v_fmac_f32_e32 v16, v87, v52
	v_fmac_f32_e32 v17, v88, v52
	v_and_b32_e32 v84, 0xffff, v79
	v_lshl_or_b32 v83, v84, 7, v89
	global_load_dwordx4 v[20:23], v83, s[12:13]
	v_lshlrev_b32_e32 v109, 1, v84
	global_load_ushort v52, v109, s[14:15]
	s_waitcnt vmcnt(6)
	v_cvt_f32_f16_e32 v53, v53
	v_cvt_f32_ubyte0_e32 v85, v24
	v_cvt_f32_ubyte1_e32 v86, v24
	v_cvt_f32_ubyte2_e32 v87, v24
	v_cvt_f32_ubyte3_e32 v88, v24
	v_fmac_f32_e32 v2, v85, v53
	v_fmac_f32_e32 v3, v86, v53
	v_fmac_f32_e32 v4, v87, v53
	v_fmac_f32_e32 v5, v88, v53
	v_cvt_f32_ubyte0_e32 v85, v25
	v_cvt_f32_ubyte1_e32 v86, v25
	v_cvt_f32_ubyte2_e32 v87, v25
	v_cvt_f32_ubyte3_e32 v88, v25
	v_fmac_f32_e32 v6, v85, v53
	v_fmac_f32_e32 v7, v86, v53
	v_fmac_f32_e32 v8, v87, v53
	v_fmac_f32_e32 v9, v88, v53
	v_cvt_f32_ubyte0_e32 v85, v26
	v_cvt_f32_ubyte1_e32 v86, v26
	v_cvt_f32_ubyte2_e32 v87, v26
	v_cvt_f32_ubyte3_e32 v88, v26
	v_fmac_f32_e32 v10, v85, v53
	v_fmac_f32_e32 v11, v86, v53
	v_fmac_f32_e32 v12, v87, v53
	v_fmac_f32_e32 v13, v88, v53
	v_cvt_f32_ubyte0_e32 v85, v27
	v_cvt_f32_ubyte1_e32 v86, v27
	v_cvt_f32_ubyte2_e32 v87, v27
	v_cvt_f32_ubyte3_e32 v88, v27
	v_fmac_f32_e32 v14, v85, v53
	v_fmac_f32_e32 v15, v86, v53
	v_fmac_f32_e32 v16, v87, v53
	v_fmac_f32_e32 v17, v88, v53
	v_lshrrev_b32_e32 v84, 16, v79
	v_lshl_or_b32 v83, v84, 7, v89
	global_load_dwordx4 v[24:27], v83, s[12:13]
	v_lshlrev_b32_e32 v109, 1, v84
	global_load_ushort v53, v109, s[14:15]
	s_waitcnt lgkmcnt(0)
	ds_bpermute_b32 v79, v90, v74 offset:24
	s_waitcnt vmcnt(6)
	v_cvt_f32_f16_e32 v54, v54
	v_cvt_f32_ubyte0_e32 v85, v28
	v_cvt_f32_ubyte1_e32 v86, v28
	v_cvt_f32_ubyte2_e32 v87, v28
	v_cvt_f32_ubyte3_e32 v88, v28
	v_fmac_f32_e32 v2, v85, v54
	v_fmac_f32_e32 v3, v86, v54
	v_fmac_f32_e32 v4, v87, v54
	v_fmac_f32_e32 v5, v88, v54
	v_cvt_f32_ubyte0_e32 v85, v29
	v_cvt_f32_ubyte1_e32 v86, v29
	v_cvt_f32_ubyte2_e32 v87, v29
	v_cvt_f32_ubyte3_e32 v88, v29
	v_fmac_f32_e32 v6, v85, v54
	v_fmac_f32_e32 v7, v86, v54
	v_fmac_f32_e32 v8, v87, v54
	v_fmac_f32_e32 v9, v88, v54
	v_cvt_f32_ubyte0_e32 v85, v30
	v_cvt_f32_ubyte1_e32 v86, v30
	v_cvt_f32_ubyte2_e32 v87, v30
	v_cvt_f32_ubyte3_e32 v88, v30
	v_fmac_f32_e32 v10, v85, v54
	v_fmac_f32_e32 v11, v86, v54
	v_fmac_f32_e32 v12, v87, v54
	v_fmac_f32_e32 v13, v88, v54
	v_cvt_f32_ubyte0_e32 v85, v31
	v_cvt_f32_ubyte1_e32 v86, v31
	v_cvt_f32_ubyte2_e32 v87, v31
	v_cvt_f32_ubyte3_e32 v88, v31
	v_fmac_f32_e32 v14, v85, v54
	v_fmac_f32_e32 v15, v86, v54
	v_fmac_f32_e32 v16, v87, v54
	v_fmac_f32_e32 v17, v88, v54
	v_and_b32_e32 v84, 0xffff, v80
	v_lshl_or_b32 v83, v84, 7, v89
	global_load_dwordx4 v[28:31], v83, s[12:13]
	v_lshlrev_b32_e32 v109, 1, v84
	global_load_ushort v54, v109, s[14:15]
	s_waitcnt vmcnt(6)
	v_cvt_f32_f16_e32 v55, v55
	v_cvt_f32_ubyte0_e32 v85, v32
	v_cvt_f32_ubyte1_e32 v86, v32
	v_cvt_f32_ubyte2_e32 v87, v32
	v_cvt_f32_ubyte3_e32 v88, v32
	v_fmac_f32_e32 v2, v85, v55
	v_fmac_f32_e32 v3, v86, v55
	v_fmac_f32_e32 v4, v87, v55
	v_fmac_f32_e32 v5, v88, v55
	v_cvt_f32_ubyte0_e32 v85, v33
	v_cvt_f32_ubyte1_e32 v86, v33
	v_cvt_f32_ubyte2_e32 v87, v33
	v_cvt_f32_ubyte3_e32 v88, v33
	v_fmac_f32_e32 v6, v85, v55
	v_fmac_f32_e32 v7, v86, v55
	v_fmac_f32_e32 v8, v87, v55
	v_fmac_f32_e32 v9, v88, v55
	v_cvt_f32_ubyte0_e32 v85, v34
	v_cvt_f32_ubyte1_e32 v86, v34
	v_cvt_f32_ubyte2_e32 v87, v34
	v_cvt_f32_ubyte3_e32 v88, v34
	v_fmac_f32_e32 v10, v85, v55
	v_fmac_f32_e32 v11, v86, v55
	v_fmac_f32_e32 v12, v87, v55
	v_fmac_f32_e32 v13, v88, v55
	v_cvt_f32_ubyte0_e32 v85, v35
	v_cvt_f32_ubyte1_e32 v86, v35
	v_cvt_f32_ubyte2_e32 v87, v35
	v_cvt_f32_ubyte3_e32 v88, v35
	v_fmac_f32_e32 v14, v85, v55
	v_fmac_f32_e32 v15, v86, v55
	v_fmac_f32_e32 v16, v87, v55
	v_fmac_f32_e32 v17, v88, v55
	v_lshrrev_b32_e32 v84, 16, v80
	v_lshl_or_b32 v83, v84, 7, v89
	global_load_dwordx4 v[32:35], v83, s[12:13]
	v_lshlrev_b32_e32 v109, 1, v84
	global_load_ushort v55, v109, s[14:15]
	s_cmp_le_u32 s40, 28
	s_cbranch_scc1 .Lg2_tail0
	s_waitcnt lgkmcnt(0)
	ds_bpermute_b32 v80, v90, v74 offset:28
	s_waitcnt vmcnt(6)
	v_cvt_f32_f16_e32 v52, v52
	v_cvt_f32_ubyte0_e32 v85, v20
	v_cvt_f32_ubyte1_e32 v86, v20
	v_cvt_f32_ubyte2_e32 v87, v20
	v_cvt_f32_ubyte3_e32 v88, v20
	v_fmac_f32_e32 v2, v85, v52
	v_fmac_f32_e32 v3, v86, v52
	v_fmac_f32_e32 v4, v87, v52
	v_fmac_f32_e32 v5, v88, v52
	v_cvt_f32_ubyte0_e32 v85, v21
	v_cvt_f32_ubyte1_e32 v86, v21
	v_cvt_f32_ubyte2_e32 v87, v21
	v_cvt_f32_ubyte3_e32 v88, v21
	v_fmac_f32_e32 v6, v85, v52
	v_fmac_f32_e32 v7, v86, v52
	v_fmac_f32_e32 v8, v87, v52
	v_fmac_f32_e32 v9, v88, v52
	v_cvt_f32_ubyte0_e32 v85, v22
	v_cvt_f32_ubyte1_e32 v86, v22
	v_cvt_f32_ubyte2_e32 v87, v22
	v_cvt_f32_ubyte3_e32 v88, v22
	v_fmac_f32_e32 v10, v85, v52
	v_fmac_f32_e32 v11, v86, v52
	v_fmac_f32_e32 v12, v87, v52
	v_fmac_f32_e32 v13, v88, v52
	v_cvt_f32_ubyte0_e32 v85, v23
	v_cvt_f32_ubyte1_e32 v86, v23
	v_cvt_f32_ubyte2_e32 v87, v23
	v_cvt_f32_ubyte3_e32 v88, v23
	v_fmac_f32_e32 v14, v85, v52
	v_fmac_f32_e32 v15, v86, v52
	v_fmac_f32_e32 v16, v87, v52
	v_fmac_f32_e32 v17, v88, v52
	v_and_b32_e32 v84, 0xffff, v79
	v_lshl_or_b32 v83, v84, 7, v89
	global_load_dwordx4 v[20:23], v83, s[12:13]
	v_lshlrev_b32_e32 v109, 1, v84
	global_load_ushort v52, v109, s[14:15]
	s_waitcnt vmcnt(6)
	v_cvt_f32_f16_e32 v53, v53
	v_cvt_f32_ubyte0_e32 v85, v24
	v_cvt_f32_ubyte1_e32 v86, v24
	v_cvt_f32_ubyte2_e32 v87, v24
	v_cvt_f32_ubyte3_e32 v88, v24
	v_fmac_f32_e32 v2, v85, v53
	v_fmac_f32_e32 v3, v86, v53
	v_fmac_f32_e32 v4, v87, v53
	v_fmac_f32_e32 v5, v88, v53
	v_cvt_f32_ubyte0_e32 v85, v25
	v_cvt_f32_ubyte1_e32 v86, v25
	v_cvt_f32_ubyte2_e32 v87, v25
	v_cvt_f32_ubyte3_e32 v88, v25
	v_fmac_f32_e32 v6, v85, v53
	v_fmac_f32_e32 v7, v86, v53
	v_fmac_f32_e32 v8, v87, v53
	v_fmac_f32_e32 v9, v88, v53
	v_cvt_f32_ubyte0_e32 v85, v26
	v_cvt_f32_ubyte1_e32 v86, v26
	v_cvt_f32_ubyte2_e32 v87, v26
	v_cvt_f32_ubyte3_e32 v88, v26
	v_fmac_f32_e32 v10, v85, v53
	v_fmac_f32_e32 v11, v86, v53
	v_fmac_f32_e32 v12, v87, v53
	v_fmac_f32_e32 v13, v88, v53
	v_cvt_f32_ubyte0_e32 v85, v27
	v_cvt_f32_ubyte1_e32 v86, v27
	v_cvt_f32_ubyte2_e32 v87, v27
	v_cvt_f32_ubyte3_e32 v88, v27
	v_fmac_f32_e32 v14, v85, v53
	v_fmac_f32_e32 v15, v86, v53
	v_fmac_f32_e32 v16, v87, v53
	v_fmac_f32_e32 v17, v88, v53
	v_lshrrev_b32_e32 v84, 16, v79
	v_lshl_or_b32 v83, v84, 7, v89
	global_load_dwordx4 v[24:27], v83, s[12:13]
	v_lshlrev_b32_e32 v109, 1, v84
	global_load_ushort v53, v109, s[14:15]
	s_waitcnt lgkmcnt(0)
	s_waitcnt vmcnt(6)
	v_cvt_f32_f16_e32 v54, v54
	v_cvt_f32_ubyte0_e32 v85, v28
	v_cvt_f32_ubyte1_e32 v86, v28
	v_cvt_f32_ubyte2_e32 v87, v28
	v_cvt_f32_ubyte3_e32 v88, v28
	v_fmac_f32_e32 v2, v85, v54
	v_fmac_f32_e32 v3, v86, v54
	v_fmac_f32_e32 v4, v87, v54
	v_fmac_f32_e32 v5, v88, v54
	v_cvt_f32_ubyte0_e32 v85, v29
	v_cvt_f32_ubyte1_e32 v86, v29
	v_cvt_f32_ubyte2_e32 v87, v29
	v_cvt_f32_ubyte3_e32 v88, v29
	v_fmac_f32_e32 v6, v85, v54
	v_fmac_f32_e32 v7, v86, v54
	v_fmac_f32_e32 v8, v87, v54
	v_fmac_f32_e32 v9, v88, v54
	v_cvt_f32_ubyte0_e32 v85, v30
	v_cvt_f32_ubyte1_e32 v86, v30
	v_cvt_f32_ubyte2_e32 v87, v30
	v_cvt_f32_ubyte3_e32 v88, v30
	v_fmac_f32_e32 v10, v85, v54
	v_fmac_f32_e32 v11, v86, v54
	v_fmac_f32_e32 v12, v87, v54
	v_fmac_f32_e32 v13, v88, v54
	v_cvt_f32_ubyte0_e32 v85, v31
	v_cvt_f32_ubyte1_e32 v86, v31
	v_cvt_f32_ubyte2_e32 v87, v31
	v_cvt_f32_ubyte3_e32 v88, v31
	v_fmac_f32_e32 v14, v85, v54
	v_fmac_f32_e32 v15, v86, v54
	v_fmac_f32_e32 v16, v87, v54
	v_fmac_f32_e32 v17, v88, v54
	v_and_b32_e32 v84, 0xffff, v80
	v_lshl_or_b32 v83, v84, 7, v89
	global_load_dwordx4 v[28:31], v83, s[12:13]
	v_lshlrev_b32_e32 v109, 1, v84
	global_load_ushort v54, v109, s[14:15]
	s_waitcnt vmcnt(6)
	v_cvt_f32_f16_e32 v55, v55
	v_cvt_f32_ubyte0_e32 v85, v32
	v_cvt_f32_ubyte1_e32 v86, v32
	v_cvt_f32_ubyte2_e32 v87, v32
	v_cvt_f32_ubyte3_e32 v88, v32
	v_fmac_f32_e32 v2, v85, v55
	v_fmac_f32_e32 v3, v86, v55
	v_fmac_f32_e32 v4, v87, v55
	v_fmac_f32_e32 v5, v88, v55
	v_cvt_f32_ubyte0_e32 v85, v33
	v_cvt_f32_ubyte1_e32 v86, v33
	v_cvt_f32_ubyte2_e32 v87, v33
	v_cvt_f32_ubyte3_e32 v88, v33
	v_fmac_f32_e32 v6, v85, v55
	v_fmac_f32_e32 v7, v86, v55
	v_fmac_f32_e32 v8, v87, v55
	v_fmac_f32_e32 v9, v88, v55
	v_cvt_f32_ubyte0_e32 v85, v34
	v_cvt_f32_ubyte1_e32 v86, v34
	v_cvt_f32_ubyte2_e32 v87, v34
	v_cvt_f32_ubyte3_e32 v88, v34
	v_fmac_f32_e32 v10, v85, v55
	v_fmac_f32_e32 v11, v86, v55
	v_fmac_f32_e32 v12, v87, v55
	v_fmac_f32_e32 v13, v88, v55
	v_cvt_f32_ubyte0_e32 v85, v35
	v_cvt_f32_ubyte1_e32 v86, v35
	v_cvt_f32_ubyte2_e32 v87, v35
	v_cvt_f32_ubyte3_e32 v88, v35
	v_fmac_f32_e32 v14, v85, v55
	v_fmac_f32_e32 v15, v86, v55
	v_fmac_f32_e32 v16, v87, v55
	v_fmac_f32_e32 v17, v88, v55
	v_lshrrev_b32_e32 v84, 16, v80
	v_lshl_or_b32 v83, v84, 7, v89
	global_load_dwordx4 v[32:35], v83, s[12:13]
	v_lshlrev_b32_e32 v109, 1, v84
	global_load_ushort v55, v109, s[14:15]
